# dilated attention: all six K/V tiles of a unit resident in LDS (LDS 160 KB), every wave runs its three tiles in three steps instead of six lockstep steps; residual epilogue counted vmcnt waits
# speedup vs baseline: 1.0242x; 1.0105x over previous
; template <class BIAS>
; __device__ __forceinline__ void attn_tiles(char* shm, const UnitIO& io, int t_begin, int t_end, const BIAS& B, int tid) {
;     const int lane = tid & 63, r32 = lane & 31, hi = lane >> 5; const int wid = __builtin_amdgcn_readfirstlane(tid >> 6);
;     const unsigned lds0 = (unsigned)(uintptr_t)shm;
;     const bf16* ksrc = io.K0 + (long)lane * io.kstride + wid * 8;
;     const bf16* vsrc = io.V0 + (long)(16 * (wid & 3) + (lane >> 2)) * io.kstride + (wid >> 2) * 32 + (lane & 3) * 8;
;     const unsigned kdst = lds0 + LDS_K + wid * 1024, vdst = lds0 + LDS_V + wid * 1024;
;     const long tstep = 64 * io.kstride;
;     ...
;     const lds_cptr shm3 = (lds_cptr)shm;
;     const lds_cptr kp0 = shm3 + LDS_K + hi * 1024 + r32 * 16;
;     const lds_cptr vp0 = shm3 + LDS_V + ((lane >> 4) & 1) * 32 + (lane & 3) * 8 + (4 * hi + ((lane & 15) >> 2)) * 64;
;     float* wsf = (float*)(shm + LDS_WS) + wid * 64;
;     bf16x8 qr[4];
;     { const bf16* qp = io.Q + (long)r32 * io.qstride + hi * 8;
; #pragma unroll
;       for (int d0 = 0; d0 < 4; ++d0) qr[d0] = *reinterpret_cast<const bf16x8*>(qp + d0 * 16); }
; __device__ __forceinline__ void dil_unit(Frame& F, const AttnBufs& A, int b, int h, int g, int r, int c) {
;     char* shm = (char*)F.lds; const int tid = F.tid, lane = tid & 63, r32 = lane & 31, hi = lane >> 5, w = F.wave;
;     const int dil = (g == 0) ? 1 : (g == 1 ? 4 : 16);
;     const int i0 = 256 * c;
;     att::BiasDil B; B.sd = exp2f(-8.0f * (float)(h - 10 + 1) / 10.0f) * LOG2E * (float)dil; B.qrel = 128 + w * 32 + r32; B.hi = hi; B.w = w; B.setup(r32);
;     const long tok_q0 = (long)b * SEQ + r + (long)dil * (i0 + w * 32);
;     const long tok_k0 = (long)b * SEQ + r + (long)dil * (i0 - 128);
;     const long bo = (long)b * (long)BADJ;
;     att::UnitIO io; io.Q = A.Q + bo + tok_q0 * DM + h * 64; io.qstride = (long)DM * dil; io.K0 = A.K + bo + tok_k0 * DM + h * 64; io.V0 = A.V + bo + tok_k0 * DM + h * 64; io.kstride = (long)DM * dil;
;     io.O = A.OD + (size_t)g * OD_BRANCH + tok_q0 * 384 + (h - 10) * 64; io.ostride = (long)384 * dil; io.L = A.LD + (size_t)g * LD_BRANCH + tok_q0 * 8 + (h - 10); io.lstride = (long)8 * dil; io.norm = false;
;     ...
;     att::attn_tiles(shm, io, 5, 6, B, tid);
;     ...
;     att::attn_tiles(shm, io, c == 0 ? 2 : 0, 6, B, tid);
.LBB0_363:
	s_lshl_b32 s56, s74, 5
	v_readlane_b32 s2, v254, 30
	s_or_b32 s56, s56, s2
	s_mul_hi_u32 s57, s56, 0xaaaaaaab
	s_lshr_b32 s75, s57, 5
	s_mul_i32 s57, s75, 48
	s_sub_i32 s66, s56, s57
	s_lshr_b32 s2, s66, 4
	s_and_b32 s67, s66, 15
	s_cmp_lt_u32 s66, 16
	s_cselect_b64 s[62:63], -1, 0
	s_cmp_eq_u32 s2, 1
	s_cselect_b64 s[64:65], -1, 0
	s_bfe_u32 s68, s66, 0x20002
	s_and_b64 s[56:57], s[64:65], exec
	s_cselect_b32 s68, s68, s67
	s_and_b64 s[56:57], s[62:63], exec
	s_cselect_b32 s68, 0, s68
	s_and_b32 s66, s66, 3
	s_and_b64 s[56:57], s[64:65], exec
	s_cselect_b32 s66, s66, 0
	s_and_b64 s[56:57], s[62:63], exec
	s_cselect_b32 s76, s67, s66
	s_and_b64 s[56:57], s[64:65], exec
	s_cselect_b32 s66, 4, 16
	s_and_b64 s[56:57], s[62:63], exec
	s_cselect_b32 s80, 1, s66
	s_not_b32 s56, s75
	s_lshl_b32 s56, s56, 3
	v_cvt_f32_i32_e32 v0, s56
	s_mov_b32 s84, 0x41200000
	s_mov_b32 s85, 0x41300000
	s_lshl_b32 s69, s76, 8
	v_div_scale_f32 v2, s[56:57], s84, s84, v0
	v_rcp_f32_e32 v3, v2
	s_mov_b32 s56, 0xc2fc0000
	v_readlane_b32 s70, v254, 38
	v_readlane_b32 s71, v254, 39
	v_fma_f32 v4, -v2, v3, 1.0
	v_fmac_f32_e32 v3, v4, v3
	v_div_scale_f32 v4, vcc, v0, s84, v0
	v_mul_f32_e32 v5, v4, v3
	v_fma_f32 v6, -v2, v5, v4
	v_fmac_f32_e32 v5, v6, v3
	v_fma_f32 v2, -v2, v5, v4
	v_div_fmas_f32 v2, v2, v3, v5
	v_div_fixup_f32 v0, v2, s84, v0
	v_cmp_gt_f32_e32 vcc, s56, v0
	s_and_b64 s[56:57], vcc, exec
	v_readlane_b32 s56, v254, 48
	s_cselect_b32 s81, 0xffffffc0, 0
	s_add_i32 s56, s69, s56
	s_or_b32 s68, s70, s68
	s_ashr_i32 s57, s56, 31
	s_and_b64 s[66:67], s[64:65], exec
	s_cselect_b32 s70, 2, 4
	s_and_b64 s[66:67], s[62:63], exec
	s_cselect_b32 s70, 0, s70
	s_lshl_b64 s[56:57], s[56:57], s70
	s_add_u32 s66, s56, s68
	s_addc_u32 s67, s57, s71
	s_add_i32 s56, s69, 0xffffff80
	s_ashr_i32 s57, s56, 31
	s_lshl_b64 s[56:57], s[56:57], s70
	s_add_u32 s56, s56, s68
	s_addc_u32 s57, s57, s71
	s_lshl_b64 s[68:69], s[66:67], 11
	v_readlane_b32 s70, v254, 42
	s_add_u32 s68, s70, s68
	v_readlane_b32 s70, v254, 45
	s_addc_u32 s69, s70, s69
	s_lshl_b32 s70, s75, 6
	s_lshl_b32 s77, s75, 7
	v_writelane_b32 v255, s70, 49
	s_add_u32 s70, s68, s77
	s_addc_u32 s71, s69, 0
	s_lshl_b64 s[68:69], s[56:57], 11
	v_readlane_b32 s56, v254, 49
	s_add_u32 s56, s56, s68
	v_readlane_b32 s57, v254, 50
	s_addc_u32 s57, s57, s69
	s_add_u32 s56, s56, s77
	s_addc_u32 s57, s57, 0
	v_readlane_b32 s78, v254, 53
	s_add_u32 s68, s78, s68
	v_readlane_b32 s78, v254, 54
	s_addc_u32 s69, s78, s69
	s_add_u32 s68, s68, s77
	s_addc_u32 s69, s69, 0
	s_cmp_eq_u32 s76, 0
	v_readfirstlane_b32 s77, v232
	s_cselect_b32 s88, 2, 0
	s_ashr_i32 s76, s77, 6
	s_and_b64 s[78:79], s[64:65], exec
	s_cselect_b32 s82, 12, 14
	s_and_b64 s[78:79], s[62:63], exec
	s_cselect_b32 s83, 10, s82
	v_lshlrev_b64 v[2:3], s83, v[146:147]
	v_lshl_add_u64 v[2:3], v[2:3], 1, s[70:71]
	v_mov_b32_e32 v149, v1
	v_lshl_add_u64 v[2:3], v[2:3], 0, v[148:149]
	flat_load_dwordx4 v[98:101], v[2:3] offset:1280
	flat_load_dwordx4 v[102:105], v[2:3] offset:1312
	flat_load_dwordx4 v[106:109], v[2:3] offset:1344
	flat_load_dwordx4 v[110:113], v[2:3] offset:1376
	v_cndmask_b32_e32 v4, 0, v224, vcc
	v_add_f32_e32 v0, v0, v4
	v_exp_f32_e32 v0, v0
	v_cvt_f32_ubyte0_e32 v3, s80
	s_mov_b32 s78, 2.0
	s_mov_b32 s79, 0x40400000
	v_ldexp_f32 v0, v0, s81
	v_mul_f32_e32 v0, 0x3fb8aa3b, v0
	v_mul_f32_e32 v155, v0, v3
	v_mov_b32_e32 v0, v155
	v_pk_mul_f32 v[158:159], v[0:1], s[78:79] op_sel_hi:[0,1]
	s_mov_b32 s78, 0x41000000
	s_mov_b32 s79, 0x41100000
	v_pk_mul_f32 v[160:161], v[0:1], s[78:79] op_sel_hi:[0,1]
	s_mov_b32 s78, 0x41800000
	s_mov_b32 s79, 0x41880000
	v_pk_mul_f32 v[164:165], v[0:1], s[78:79] op_sel_hi:[0,1]
	s_mov_b32 s78, 0x41900000
	s_mov_b32 s79, 0x41980000
	v_pk_mul_f32 v[166:167], v[0:1], s[78:79] op_sel_hi:[0,1]
	s_mov_b32 s78, 0x41c00000
	s_mov_b32 s79, 0x41c80000
	v_pk_mul_f32 v[168:169], v[0:1], s[78:79] op_sel_hi:[0,1]
	s_mov_b32 s78, 0x41d00000
	s_mov_b32 s79, 0x41d80000
	v_pk_mul_f32 v[170:171], v[0:1], s[78:79] op_sel_hi:[0,1]
	s_lshl_b32 s70, s76, 4
	s_ashr_i32 s79, s77, 3
	v_pk_mul_f32 v[162:163], v[0:1], s[84:85] op_sel_hi:[0,1]
	s_lshl_b32 s80, s76, 3
	s_lshl_b32 s78, s76, 10
	v_and_or_b32 v0, s70, 48, v178
	s_and_b32 s82, s79, 0xffffffe0
	v_lshlrev_b64 v[4:5], s83, v[194:195]
	s_ashr_i32 s81, s80, 31
	s_add_i32 s79, s78, 0x8000
	v_lshlrev_b64 v[6:7], s83, v[0:1]
	s_ashr_i32 s83, s82, 31
	v_lshl_add_u64 v[4:5], v[4:5], 1, s[56:57]
	s_and_b64 s[56:57], s[64:65], exec
	v_lshl_add_u64 v[172:173], s[80:81], 1, v[4:5]
	v_lshlrev_b32_e32 v248, 11, v246
	v_mov_b32_e32 v249, s2
	v_lshlrev_b32_e32 v249, 1, v249
	v_lshlrev_b32_e32 v248, v249, v248
	v_add_u32_e32 v248, v248, v247
	v_ashrrev_i32_e32 v249, 31, v248
	v_lshl_add_u64 v[172:173], v[172:173], 0, v[248:249]
	v_lshl_add_u64 v[4:5], v[6:7], 1, s[68:69]
	s_cselect_b32 s68, 18, 20
	s_and_b64 s[56:57], s[62:63], exec
	s_mov_b32 s89, s3
	s_cselect_b32 s80, 16, s68
	v_mov_b32_e32 v151, v1
	v_lshl_add_u64 v[4:5], s[82:83], 1, v[4:5]
	v_lshl_add_u64 v[174:175], v[4:5], 0, v[150:151]
	v_writelane_b32 v254, s2, 9
	v_mov_b32_e32 v2, 0
	s_mov_b32 s81, s88
	s_mov_b32 s100, s88
; #define ATT_WAIT_BAR(N) asm volatile("s_waitcnt vmcnt(" #N ") lgkmcnt(0)\n\ts_barrier" ::: "memory")
; #define ATT_DMA(t, slot) do { glds16(ksrc + (long)(t) * tstep, (unsigned)__builtin_amdgcn_readfirstlane(kdst + (slot))); glds16(vsrc + (long)(t) * tstep, (unsigned)__builtin_amdgcn_readfirstlane(vdst + (slot))); } while (0)
;     __device__ __forceinline__ void init(f32x16& c0, f32x16& c1, int t) const {
;         const int dt = t - (w >> 1);
;         const float base = basel + (float)dt * d64;
; #pragma unroll
;         for (int i = 0; i < 8; ++i) { const f32x2_t p = kc[i] + base, q = p + d32; c0[2 * i] = p[0]; c0[2 * i + 1] = p[1]; c1[2 * i] = q[0]; c1[2 * i + 1] = q[1]; }
;         if (dt == 0) {
; #pragma unroll
;             for (int r = 0; r < 16; ++r) { const int ko = (r & 3) + 8 * (r >> 2); if (ko < u) c0[r] = ATT_NEG; if (ko < u - 32) c1[r] = ATT_NEG; }
; template <class BIAS>
; __device__ __forceinline__ void attn_tiles(char* shm, const UnitIO& io, int t_begin, int t_end, const BIAS& B, int tid) {
;     ...
;     ATT_DMA(t_begin, 0);
;     asm volatile("" :: "v"(qr[0]), "v"(qr[1]), "v"(qr[2]), "v"(qr[3]));
;     const int nt_ = t_end - t_begin; if (nt_ > 1) ATT_DMA(t_begin + 1, SLOTB); if (nt_ > 2) ATT_DMA(t_begin + 2, 2 * SLOTB);
;     f32x16 o[2]; o[0] = f32x16{}; o[1] = f32x16{}; float l_reg = 0.f;
;     if (nt_ > 2) ATT_WAIT_BAR(4); else if (nt_ > 1) ATT_WAIT_BAR(2); else ATT_WAIT_BAR(0);
; #pragma unroll 1
;     for (int t = t_begin; t < t_end; ++t) {
;         const int rem = t_end - t;
;         const bool act = B.active(t);
;         const int sl_c = ((t - t_begin) & 3) * SLOTB;
;         if (rem > 3) ATT_DMA(t + 3, ((t + 3 - t_begin) & 3) * SLOTB);
.Ldl_pro:
	s_mov_b32 s101, 0
	s_lshl_b64 s[56:57], s[100:101], s80
	s_lshl_b64 s[56:57], s[56:57], 1
	s_add_u32 s56, s56, 0x500
	s_addc_u32 s57, s57, 0
	v_lshl_add_u64 v[4:5], v[172:173], 0, s[56:57]
	v_lshl_add_u64 v[6:7], v[174:175], 0, s[56:57]
	s_lshl_b32 s68, s100, 13
	s_cmp_gt_u32 s100, 3
	s_cselect_b32 s69, 0x14000, 0
	s_add_i32 s68, s68, s69
	s_add_i32 s69, s68, s78
	s_mov_b32 m0, s69
	s_add_i32 s68, s68, s79
	global_load_lds_dwordx4 v[4:5], off
	s_mov_b32 m0, s68
	s_nop 0
	global_load_lds_dwordx4 v[6:7], off
	s_add_i32 s100, s100, 1
	s_cmp_lt_u32 s100, 6
	s_cbranch_scc1 .Ldl_pro
	s_mov_b32 s88, s73
	s_waitcnt vmcnt(4) lgkmcnt(0)
	s_barrier
	v_mov_b32_e32 v16, v2
	v_mov_b32_e32 v17, v2
	v_mul_f32_e32 v156, 0x42000000, v155
	v_mov_b32_e32 v3, v2
	v_mov_b32_e32 v4, v2
	v_mov_b32_e32 v5, v2
	v_mov_b32_e32 v6, v2
	v_mov_b32_e32 v7, v2
	v_mov_b32_e32 v8, v2
	v_mov_b32_e32 v9, v2
	v_mov_b32_e32 v10, v2
	v_mov_b32_e32 v11, v2
	v_mov_b32_e32 v12, v2
	v_mov_b32_e32 v13, v2
	v_mov_b32_e32 v14, v2
	v_mov_b32_e32 v15, v2
	v_mov_b64_e32 v[32:33], v[16:17]
	v_mul_f32_e32 v149, 0x42800000, v155
	v_mul_f32_e32 v154, 0, v155
	v_writelane_b32 v254, s3, 10
	v_mul_f32_e32 v0, v155, v196
	v_mov_b32_e32 v176, v156
	v_mov_b32_e32 v177, v156
	v_mov_b64_e32 v[30:31], v[14:15]
	v_mov_b64_e32 v[28:29], v[12:13]
	v_mov_b64_e32 v[26:27], v[10:11]
	v_mov_b64_e32 v[24:25], v[8:9]
	v_mov_b64_e32 v[22:23], v[6:7]
	v_mov_b64_e32 v[20:21], v[4:5]
	v_mov_b64_e32 v[18:19], v[2:3]
	v_mov_b32_e32 v151, v2
	s_branch .LBB0_365
.LBB0_364:
	s_add_i32 s88, s88, 1
	s_cmp_gt_i32 s88, s33
	s_cbranch_scc1 .LBB0_389
.LBB0_365:
	s_lshl_b32 s82, s88, 13
	s_cmp_gt_u32 s88, 3
	s_cselect_b32 s56, 0x14000, 0
	s_add_i32 s82, s82, s56
	s_cmp_lt_i32 s88, s81
	s_cbranch_scc1 .Ldl_endstep
	v_add_u32_e32 v34, s82, v240
	v_add_u32_e32 v35, s82, v241
	v_add_u32_e32 v36, s82, v242
	v_add_u32_e32 v37, s82, v243
	ds_read_b128 v[130:133], v34
	ds_read_b128 v[126:129], v34 offset:4096
	ds_read_b128 v[134:137], v35
	ds_read_b128 v[122:125], v35 offset:4096
	ds_read_b128 v[138:141], v36
	ds_read_b128 v[118:121], v36 offset:4096
	ds_read_b128 v[142:145], v37
	ds_read_b128 v[114:117], v37 offset:4096
	s_add_u32 s70, s72, s88
	v_cvt_f32_i32_e32 v34, s70
	v_mov_b32_e32 v157, v156
	v_fma_f32 v34, v149, v34, -v0
	v_add_f32_e32 v82, v154, v34
	v_add_f32_e32 v83, v155, v34
	v_add_f32_e32 v84, v158, v34
	v_add_f32_e32 v85, v159, v34
	v_add_f32_e32 v86, v160, v34
	v_add_f32_e32 v87, v161, v34
	v_add_f32_e32 v88, v162, v34
	v_add_f32_e32 v89, v163, v34
	v_add_f32_e32 v90, v164, v34
	v_add_f32_e32 v91, v165, v34
	v_add_f32_e32 v92, v166, v34
	v_add_f32_e32 v93, v167, v34
	v_add_f32_e32 v94, v168, v34
	v_add_f32_e32 v95, v169, v34
	v_add_f32_e32 v96, v170, v34
	v_add_f32_e32 v97, v171, v34
	v_add_f32_e32 v46, v156, v94
	v_add_f32_e32 v47, v157, v95
	v_add_f32_e32 v48, v156, v96
	v_add_f32_e32 v49, v157, v97
	v_add_f32_e32 v44, v156, v92
	v_add_f32_e32 v45, v157, v93
	v_add_f32_e32 v42, v156, v90
	v_add_f32_e32 v43, v157, v91
	v_add_f32_e32 v40, v156, v88
	v_add_f32_e32 v41, v157, v89
	v_add_f32_e32 v38, v156, v86
	v_add_f32_e32 v39, v157, v87
	v_add_f32_e32 v36, v156, v84
	v_add_f32_e32 v37, v157, v85
	v_add_f32_e32 v34, v176, v82
	v_add_f32_e32 v35, v177, v83
	s_cmp_eq_u32 s70, 1
	s_cbranch_scc1 .Ldil_h1_go
	s_cmp_eq_u32 s70, 0
	s_cbranch_scc0 .Ldil_m2
	v_cndmask_b32_e64 v82, v82, v226, s[6:7]
	v_cndmask_b32_e64 v83, v83, v226, s[10:11]
	v_cndmask_b32_e64 v84, v84, v226, s[14:15]
	v_cndmask_b32_e64 v85, v85, v226, s[18:19]
	v_cndmask_b32_e64 v86, v86, v226, s[22:23]
	v_cndmask_b32_e64 v87, v87, v226, s[26:27]
	v_cndmask_b32_e64 v88, v88, v226, s[92:93]
	v_cndmask_b32_e64 v89, v89, v226, s[96:97]
	v_cndmask_b32_e64 v90, v90, v226, s[4:5]
	v_cndmask_b32_e64 v91, v91, v226, s[60:61]
	v_cndmask_b32_e64 v92, v92, v226, s[30:31]
	v_cndmask_b32_e64 v93, v93, v226, s[58:59]
	v_cndmask_b32_e64 v94, v94, v226, s[40:41]
	v_cndmask_b32_e64 v95, v95, v226, s[44:45]
	v_cndmask_b32_e64 v96, v96, v226, s[48:49]
	v_cndmask_b32_e64 v34, v34, v226, s[8:9]
	v_cndmask_b32_e64 v35, v35, v226, s[12:13]
	v_cndmask_b32_e64 v36, v36, v226, s[16:17]
	v_cndmask_b32_e64 v37, v37, v226, s[20:21]
	v_cndmask_b32_e64 v38, v38, v226, s[24:25]
	v_cndmask_b32_e64 v39, v39, v226, s[90:91]
	v_cndmask_b32_e64 v40, v40, v226, s[94:95]
	v_cndmask_b32_e64 v41, v41, v226, s[34:35]
	v_cndmask_b32_e64 v42, v42, v226, s[0:1]
	v_cndmask_b32_e64 v43, v43, v226, s[28:29]
	v_cndmask_b32_e64 v44, v44, v226, s[36:37]
	v_cndmask_b32_e64 v45, v45, v226, s[38:39]
	v_cndmask_b32_e64 v46, v46, v226, s[42:43]
	v_cndmask_b32_e64 v47, v47, v226, s[46:47]
	v_cndmask_b32_e64 v48, v48, v226, s[50:51]
	v_cndmask_b32_e64 v97, v97, v226, s[52:53]
	v_cndmask_b32_e64 v49, v49, v226, s[54:55]
	s_branch .Ldil_h1_go
;     __device__ __forceinline__ void init(f32x16& c0, f32x16& c1, int t) const {
;     ...
;         } else if (dt == 2) {
; #pragma unroll
;             for (int r = 0; r < 16; ++r) { const int ko = (r & 3) + 8 * (r >> 2); if (ko > u) c0[r] = ATT_NEG; if (ko > u - 32) c1[r] = ATT_NEG; }
;         }
.Ldil_m2:
	s_and_b32 s2, s76, 1
	s_lshl_b32 s2, s2, 5
	v_lshrrev_b32_e32 v51, 3, v194
	v_and_b32_e32 v51, 4, v51
	v_add_u32_e32 v50, s2, v146
	v_sub_u32_e32 v50, v50, v51
	v_add_u32_e32 v51, 0xffffffe0, v50
	v_cmp_gt_i32_e64 s[2:3], 0, v50
	v_cmp_gt_i32_e64 s[70:71], 1, v50
	v_cmp_gt_i32_e64 s[84:85], 2, v50
	v_cndmask_b32_e64 v82, v82, v226, s[2:3]
	v_cndmask_b32_e64 v83, v83, v226, s[70:71]
	v_cndmask_b32_e64 v84, v84, v226, s[84:85]
	v_cmp_gt_i32_e64 s[2:3], 3, v50
	v_cmp_gt_i32_e64 s[70:71], 8, v50
	v_cmp_gt_i32_e64 s[84:85], 9, v50
	v_cndmask_b32_e64 v85, v85, v226, s[2:3]
	v_cndmask_b32_e64 v86, v86, v226, s[70:71]
	v_cndmask_b32_e64 v87, v87, v226, s[84:85]
	v_cmp_gt_i32_e64 s[2:3], 10, v50
	v_cmp_gt_i32_e64 s[70:71], 11, v50
	v_cmp_gt_i32_e64 s[84:85], 16, v50
	v_cndmask_b32_e64 v88, v88, v226, s[2:3]
	v_cndmask_b32_e64 v89, v89, v226, s[70:71]
	v_cndmask_b32_e64 v90, v90, v226, s[84:85]
	v_cmp_gt_i32_e64 s[2:3], 17, v50
	v_cmp_gt_i32_e64 s[70:71], 18, v50
	v_cmp_gt_i32_e64 s[84:85], 19, v50
	v_cndmask_b32_e64 v91, v91, v226, s[2:3]
	v_cndmask_b32_e64 v92, v92, v226, s[70:71]
	v_cndmask_b32_e64 v93, v93, v226, s[84:85]
	v_cmp_gt_i32_e64 s[2:3], 24, v50
	v_cmp_gt_i32_e64 s[70:71], 25, v50
	v_cmp_gt_i32_e64 s[84:85], 26, v50
	v_cndmask_b32_e64 v94, v94, v226, s[2:3]
	v_cndmask_b32_e64 v95, v95, v226, s[70:71]
	v_cndmask_b32_e64 v96, v96, v226, s[84:85]
	v_cmp_gt_i32_e64 s[2:3], 27, v50
	v_cmp_gt_i32_e64 s[70:71], 0, v51
	v_cmp_gt_i32_e64 s[84:85], 1, v51
	v_cndmask_b32_e64 v97, v97, v226, s[2:3]
	v_cndmask_b32_e64 v34, v34, v226, s[70:71]
	v_cndmask_b32_e64 v35, v35, v226, s[84:85]
	v_cmp_gt_i32_e64 s[2:3], 2, v51
	v_cmp_gt_i32_e64 s[70:71], 3, v51
	v_cmp_gt_i32_e64 s[84:85], 8, v51
	v_cndmask_b32_e64 v36, v36, v226, s[2:3]
	v_cndmask_b32_e64 v37, v37, v226, s[70:71]
	v_cndmask_b32_e64 v38, v38, v226, s[84:85]
	v_cmp_gt_i32_e64 s[2:3], 9, v51
	v_cmp_gt_i32_e64 s[70:71], 10, v51
	v_cmp_gt_i32_e64 s[84:85], 11, v51
	v_cndmask_b32_e64 v39, v39, v226, s[2:3]
	v_cndmask_b32_e64 v40, v40, v226, s[70:71]
	v_cndmask_b32_e64 v41, v41, v226, s[84:85]
	v_cmp_gt_i32_e64 s[2:3], 16, v51
	v_cmp_gt_i32_e64 s[70:71], 17, v51
	v_cmp_gt_i32_e64 s[84:85], 18, v51
	v_cndmask_b32_e64 v42, v42, v226, s[2:3]
	v_cndmask_b32_e64 v43, v43, v226, s[70:71]
	v_cndmask_b32_e64 v44, v44, v226, s[84:85]
	v_cmp_gt_i32_e64 s[2:3], 19, v51
	v_cmp_gt_i32_e64 s[70:71], 24, v51
	v_cmp_gt_i32_e64 s[84:85], 25, v51
	v_cndmask_b32_e64 v45, v45, v226, s[2:3]
	v_cndmask_b32_e64 v46, v46, v226, s[70:71]
	v_cndmask_b32_e64 v47, v47, v226, s[84:85]
	v_cmp_gt_i32_e64 s[2:3], 26, v51
	v_cmp_gt_i32_e64 s[70:71], 27, v51
	s_nop 0
	v_cndmask_b32_e64 v48, v48, v226, s[2:3]
	v_cndmask_b32_e64 v49, v49, v226, s[70:71]
	s_branch .Ldil_h1_go
; #define ATT_WAIT_BAR(N) asm volatile("s_waitcnt vmcnt(" #N ") lgkmcnt(0)\n\ts_barrier" ::: "memory")
; __device__ __forceinline__ unsigned cvtpk(float lo, float hi) { f32x2_t v = {lo, hi}; bf16x2_t b = __builtin_convertvector(v, bf16x2_t); return __builtin_bit_cast(unsigned, b); }
; template <class BIAS>
; __device__ __forceinline__ void attn_tiles(char* shm, const UnitIO& io, int t_begin, int t_end, const BIAS& B, int tid) {
;     ...
;         if (act) {
;             const lds_cptr vp = vp0 + sl_c;
;             s16x4 vlo[8], vhi[8];
; #pragma unroll
;             for (int i = 0; i < 8; ++i) { vlo[i] = vtr(vp + (i >> 2) * 4096 + (i & 3) * 1024); vhi[i] = vtr(vp + (i >> 2) * 4096 + (i & 3) * 1024 + 512); }
;             ATT_SBAR();
;             { float s1 = 0.f;
; #pragma unroll
;               for (int r = 0; r < 16; ++r) c1x[r] = __builtin_amdgcn_exp2f(c1x[r]);
;               { f32x2_t s2 = (f32x2_t){c1x[0], c1x[1]};
; #pragma unroll
;                 for (int i = 1; i < 8; ++i) s2 += (f32x2_t){c1x[2 * i], c1x[2 * i + 1]};
;                 s1 = s2[0] + s2[1]; }
;               l_reg += s1;
; #pragma unroll
;               for (int i = 0; i < 4; ++i) { pw[2][i] = cvtpk(c1x[2 * i], c1x[2 * i + 1]); pw[3][i] = cvtpk(c1x[8 + 2 * i], c1x[9 + 2 * i]); } }
;             ATT_SBAR();
;             asm volatile("" : "+v"(vlo[0]), "+v"(vhi[0]), "+v"(vlo[1]), "+v"(vhi[1]), "+v"(vlo[2]), "+v"(vhi[2]), "+v"(vlo[3]), "+v"(vhi[3]));
; #pragma unroll
;             for (int ks = 0; ks < 4; ++ks) { const bf16x8 vf = (bf16x8){vlo[ks][0], vlo[ks][1], vlo[ks][2], vlo[ks][3], vhi[ks][0], vhi[ks][1], vhi[ks][2], vhi[ks][3]};
;                 o[0] = __builtin_amdgcn_mfma_f32_32x32x16_bf16(__builtin_bit_cast(bf16x8, pw[ks]), vf, o[0], 0, 0, 0); }
;             ATT_SBAR();
;             asm volatile("" : "+v"(vlo[4]), "+v"(vhi[4]), "+v"(vlo[5]), "+v"(vhi[5]), "+v"(vlo[6]), "+v"(vhi[6]), "+v"(vlo[7]), "+v"(vhi[7]));
; #pragma unroll
;             for (int ks = 0; ks < 4; ++ks) { const bf16x8 vf = (bf16x8){vlo[4 + ks][0], vlo[4 + ks][1], vlo[4 + ks][2], vlo[4 + ks][3], vhi[4 + ks][0], vhi[4 + ks][1], vhi[4 + ks][2], vhi[4 + ks][3]};
;                 o[1] = __builtin_amdgcn_mfma_f32_32x32x16_bf16(__builtin_bit_cast(bf16x8, pw[ks]), vf, o[1], 0, 0, 0); }
;         }
;         if (rem > 3) ATT_WAIT_BAR(4); else if (rem > 2) ATT_WAIT_BAR(2); else ATT_WAIT_BAR(0);
.LBB0_375:
	v_add_u32_e32 v88, s82, v180
	ds_read_b64_tr_b16 v[58:59], v88 offset:32768
	ds_read_b64_tr_b16 v[60:61], v88 offset:33280
	ds_read_b64_tr_b16 v[62:63], v88 offset:33792
	ds_read_b64_tr_b16 v[64:65], v88 offset:34304
	ds_read_b64_tr_b16 v[66:67], v88 offset:34816
	ds_read_b64_tr_b16 v[68:69], v88 offset:35328
	ds_read_b64_tr_b16 v[70:71], v88 offset:35840
	ds_read_b64_tr_b16 v[72:73], v88 offset:36352
	ds_read_b64_tr_b16 v[74:75], v88 offset:36864
	ds_read_b64_tr_b16 v[76:77], v88 offset:37376
	ds_read_b64_tr_b16 v[78:79], v88 offset:37888
	ds_read_b64_tr_b16 v[80:81], v88 offset:38400
	ds_read_b64_tr_b16 v[82:83], v88 offset:38912
	ds_read_b64_tr_b16 v[84:85], v88 offset:39424
	ds_read_b64_tr_b16 v[86:87], v88 offset:39936
	ds_read_b64_tr_b16 v[88:89], v88 offset:40448
	v_exp_f32_e32 v34, v34
	v_exp_f32_e32 v35, v35
	v_exp_f32_e32 v36, v36
	v_exp_f32_e32 v37, v37
	s_waitcnt lgkmcnt(14)
	v_mfma_f32_32x32x16_bf16 v[2:17], v[50:53], v[58:61], v[2:17]
	v_exp_f32_e32 v38, v38
	v_exp_f32_e32 v39, v39
	v_exp_f32_e32 v40, v40
	v_exp_f32_e32 v41, v41
	s_waitcnt lgkmcnt(12)
	v_mfma_f32_32x32x16_bf16 v[2:17], v[54:57], v[62:65], v[2:17]
	v_exp_f32_e32 v42, v42
	v_exp_f32_e32 v43, v43
	v_exp_f32_e32 v44, v44
	v_exp_f32_e32 v45, v45
	s_waitcnt lgkmcnt(6)
	v_mfma_f32_32x32x16_bf16 v[18:33], v[50:53], v[74:77], v[18:33]
	v_add_f32_e32 v90, v36, v34
	v_add_f32_e32 v91, v37, v35
	v_exp_f32_e32 v46, v46
	v_exp_f32_e32 v47, v47
	s_waitcnt lgkmcnt(4)
	v_mfma_f32_32x32x16_bf16 v[18:33], v[54:57], v[78:81], v[18:33]
	v_add_f32_e32 v90, v38, v90
	v_add_f32_e32 v91, v39, v91
	v_exp_f32_e32 v48, v48
	v_exp_f32_e32 v49, v49
	v_add_f32_e32 v90, v40, v90
	v_add_f32_e32 v91, v41, v91
	v_cvt_pk_bf16_f32 v94, v42, v43
	v_add_f32_e32 v90, v42, v90
	v_add_f32_e32 v91, v43, v91
	v_cvt_pk_bf16_f32 v95, v44, v45
	v_add_f32_e32 v90, v44, v90
	v_add_f32_e32 v91, v45, v91
	v_cvt_pk_bf16_f32 v92, v38, v39
	v_add_f32_e32 v90, v46, v90
	v_add_f32_e32 v91, v47, v91
	v_cvt_pk_bf16_f32 v96, v46, v47
	v_add_f32_e32 v90, v48, v90
	v_add_f32_e32 v91, v49, v91
	v_cvt_pk_bf16_f32 v93, v40, v41
	v_add_f32_e32 v114, v90, v91
	v_cvt_pk_bf16_f32 v90, v34, v35
	v_cvt_pk_bf16_f32 v91, v36, v37
	v_cvt_pk_bf16_f32 v97, v48, v49
	s_waitcnt lgkmcnt(0)
	s_nop 0
	v_mfma_f32_32x32x16_bf16 v[2:17], v[90:93], v[66:69], v[2:17]
	v_mfma_f32_32x32x16_bf16 v[2:17], v[94:97], v[70:73], v[2:17]
	v_add_f32_e32 v151, v151, v114
	v_mfma_f32_32x32x16_bf16 v[18:33], v[90:93], v[82:85], v[18:33]
	v_mfma_f32_32x32x16_bf16 v[18:33], v[94:97], v[86:89], v[18:33]
.Ldl_endstep:
	s_add_i32 s56, s72, s88
	s_cmp_lg_u32 s56, 0
	s_cbranch_scc1 .Ldl_w0
	s_waitcnt vmcnt(2) lgkmcnt(0)
	s_barrier
	s_branch .LBB0_364
.Ldl_w0:
	s_waitcnt vmcnt(0) lgkmcnt(0)
	s_barrier
	s_branch .LBB0_364
.Ldil_h1_go:
	s_waitcnt lgkmcnt(0)
	s_nop 0
	v_mfma_f32_32x32x16_bf16 v[82:97], v[130:133], v[98:101], v[82:97]
	v_mfma_f32_32x32x16_bf16 v[82:97], v[134:137], v[102:105], v[82:97]
	v_mfma_f32_32x32x16_bf16 v[82:97], v[138:141], v[106:109], v[82:97]
	v_mfma_f32_32x32x16_bf16 v[82:97], v[142:145], v[110:113], v[82:97]
	v_mfma_f32_32x32x16_bf16 v[34:49], v[126:129], v[98:101], v[34:49]
	s_nop 10
.Ldl_go:
	v_exp_f32_e32 v50, v82
	v_exp_f32_e32 v51, v83
	v_exp_f32_e32 v52, v84
	v_exp_f32_e32 v53, v85
	v_mfma_f32_32x32x16_bf16 v[34:49], v[122:125], v[102:105], v[34:49]
	v_exp_f32_e32 v56, v86
	v_exp_f32_e32 v57, v87
	v_exp_f32_e32 v58, v88
	v_exp_f32_e32 v59, v89
	v_mfma_f32_32x32x16_bf16 v[34:49], v[118:121], v[106:109], v[34:49]
	v_exp_f32_e32 v54, v90
	v_exp_f32_e32 v55, v91
	v_exp_f32_e32 v60, v92
	v_exp_f32_e32 v61, v93
	v_mfma_f32_32x32x16_bf16 v[34:49], v[114:117], v[110:113], v[34:49]
	v_add_f32_e32 v66, v50, v52
	v_add_f32_e32 v67, v51, v53
	v_exp_f32_e32 v62, v94
	v_exp_f32_e32 v63, v95
	v_add_f32_e32 v66, v56, v66
	v_add_f32_e32 v67, v57, v67
	v_exp_f32_e32 v64, v96
	v_exp_f32_e32 v65, v97
	v_add_f32_e32 v66, v58, v66
	v_add_f32_e32 v67, v59, v67
	v_cvt_pk_bf16_f32 v50, v50, v51
	v_add_f32_e32 v66, v54, v66
	v_add_f32_e32 v67, v55, v67
	v_cvt_pk_bf16_f32 v54, v54, v55
	v_add_f32_e32 v66, v60, v66
	v_add_f32_e32 v67, v61, v67
	v_cvt_pk_bf16_f32 v51, v52, v53
	v_add_f32_e32 v66, v62, v66
	v_add_f32_e32 v67, v63, v67
	v_cvt_pk_bf16_f32 v55, v60, v61
	v_add_f32_e32 v66, v64, v66
	v_add_f32_e32 v67, v65, v67
	v_cvt_pk_bf16_f32 v52, v56, v57
	v_add_f32_e32 v66, v66, v67
	v_cvt_pk_bf16_f32 v56, v62, v63
	v_cvt_pk_bf16_f32 v53, v58, v59
	v_cvt_pk_bf16_f32 v57, v64, v65
	v_add_f32_e32 v151, v151, v66
	s_branch .LBB0_375

; #define PG8_GAS __attribute__((address_space(1)))
; #define PG8_PACK8(y0, y1) (u32x4){cvt_pk_bf16((y0)[0], (y0)[1]), cvt_pk_bf16((y0)[2], (y0)[3]), cvt_pk_bf16((y1)[0], (y1)[1]), cvt_pk_bf16((y1)[2], (y1)[3])}
;     __device__ __forceinline__ void operator()(const f32x4 (&acc)[2][2][4][2], const Unit& u, int ui, int wr, int wc, int fr, int fq) const {
;     ...
;                 for (int bj = 0; bj < 2; ++bj) { const unsigned off = (row0 + ai * HALF + m * 16) * 1024u + col0 + bj * HALF;
;                     xw[ai][m][bj] = *(const PG8_GAS u32x4*)((PG8_GAS unsigned char*)ws + E_XB + (size_t)(off * 2u)); }
;         float ssv[2][4];
; #pragma unroll
;         for (int ai = 0; ai < 2; ++ai) {
; #pragma unroll
;             for (int m = 0; m < 4; ++m) {
;                 const unsigned row = row0 + ai * HALF + m * 16; float ss = 0.f;
; #pragma unroll
;                 for (int bj = 0; bj < 2; ++bj) {
;                     const unsigned off = row * 1024u + col0 + bj * HALF;
;                     const u32x4 x4 = xw[ai][m][bj];
;                     f32x4 o0, o1;
;                     o0[0] = __builtin_bit_cast(float, x4[0] << 16) + acc[ai][bj][m][0][0]; o0[1] = __builtin_bit_cast(float, x4[0] & 0xffff0000u) + acc[ai][bj][m][0][1];
;                     o0[2] = __builtin_bit_cast(float, x4[1] << 16) + acc[ai][bj][m][0][2]; o0[3] = __builtin_bit_cast(float, x4[1] & 0xffff0000u) + acc[ai][bj][m][0][3];
;                     o1[0] = __builtin_bit_cast(float, x4[2] << 16) + acc[ai][bj][m][1][0]; o1[1] = __builtin_bit_cast(float, x4[2] & 0xffff0000u) + acc[ai][bj][m][1][1];
;                     o1[2] = __builtin_bit_cast(float, x4[3] << 16) + acc[ai][bj][m][1][2]; o1[3] = __builtin_bit_cast(float, x4[3] & 0xffff0000u) + acc[ai][bj][m][1][3];
;                     if (last) { __builtin_nontemporal_store(o0, (PG8_GAS f32x4*)((PG8_GAS float*)out + (size_t)off)); __builtin_nontemporal_store(o1, (PG8_GAS f32x4*)((PG8_GAS float*)out + (size_t)off + 4)); }
;                     else {
;                         const f32x4 q4 = o0 * o0 + o1 * o1; ss += (q4[0] + q4[1]) + (q4[2] + q4[3]);
;                         *(PG8_GAS u32x4*)((PG8_GAS unsigned char*)ws + E_XB + (size_t)(off * 2u)) = PG8_PACK8(o0, o1);
.LBB0_421:
	v_lshl_or_b32 v0, s4, 8, v210
	v_lshl_add_u32 v213, s0, 8, v195
	v_lshlrev_b32_e32 v74, 1, v0
	v_lshl_add_u32 v74, v213, 11, v74
	v_or_b32_e32 v75, 0x100, v74
	global_load_dwordx4 v[218:221], v74, s[12:13]
	global_load_dwordx4 v[186:189], v75, s[12:13]
	v_add_u32_e32 v75, 0x8000, v74
	global_load_dwordx4 v[182:185], v75, s[12:13]
	v_add_u32_e32 v75, 0x8100, v74
	global_load_dwordx4 v[178:181], v75, s[12:13]
	v_add_u32_e32 v75, 0x10000, v74
	global_load_dwordx4 v[174:177], v75, s[12:13]
	v_add_u32_e32 v75, 0x10100, v74
	global_load_dwordx4 v[170:173], v75, s[12:13]
	v_add_u32_e32 v75, 0x18000, v74
	global_load_dwordx4 v[166:169], v75, s[12:13]
	v_add_u32_e32 v75, 0x18100, v74
	global_load_dwordx4 v[154:157], v75, s[12:13]
	v_add_u32_e32 v75, 0x40000, v74
	global_load_dwordx4 v[150:153], v75, s[12:13]
	v_add_u32_e32 v75, 0x40100, v74
	global_load_dwordx4 v[142:145], v75, s[12:13]
	v_add_u32_e32 v75, 0x48000, v74
	global_load_dwordx4 v[126:129], v75, s[12:13]
	v_add_u32_e32 v75, 0x48100, v74
	global_load_dwordx4 v[122:125], v75, s[12:13]
	v_add_u32_e32 v75, 0x50000, v74
	global_load_dwordx4 v[106:109], v75, s[12:13]
	v_add_u32_e32 v75, 0x50100, v74
	global_load_dwordx4 v[98:101], v75, s[12:13]
	v_add_u32_e32 v75, 0x58000, v74
	v_add_u32_e32 v74, 0x58100, v74
	global_load_dwordx4 v[86:89], v75, s[12:13]
	v_lshl_add_u32 v0, v213, 10, v0
	global_load_dwordx4 v[74:77], v74, s[12:13]
	s_mov_b64 s[0:1], -1
	s_and_b64 vcc, exec, s[8:9]
	s_waitcnt vmcnt(15)
	v_lshlrev_b32_e32 v190, 16, v218
	v_and_b32_e32 v191, 0xffff0000, v218
	v_pk_add_f32 v[162:163], v[162:163], v[190:191]
	v_lshlrev_b32_e32 v190, 16, v219
	v_and_b32_e32 v191, 0xffff0000, v219
	v_pk_add_f32 v[164:165], v[164:165], v[190:191]
	v_lshlrev_b32_e32 v190, 16, v220
	v_and_b32_e32 v191, 0xffff0000, v220
	v_pk_add_f32 v[158:159], v[158:159], v[190:191]
	v_lshlrev_b32_e32 v190, 16, v221
	v_and_b32_e32 v191, 0xffff0000, v221
	v_pk_add_f32 v[160:161], v[160:161], v[190:191]
	s_cbranch_vccz .LBB0_423
	v_pk_mul_f32 v[190:191], v[160:161], v[160:161]
	v_pk_mul_f32 v[218:219], v[158:159], v[158:159]
	v_pk_fma_f32 v[190:191], v[164:165], v[164:165], v[190:191]
	v_pk_fma_f32 v[218:219], v[162:163], v[162:163], v[218:219]
	s_mov_b64 s[0:1], 0
	v_pk_mov_b32 v[220:221], v[218:219], v[190:191] op_sel:[1,0]
	v_mov_b32_e32 v219, v191
	v_pk_add_f32 v[190:191], v[220:221], v[218:219]
	v_cvt_pk_bf16_f32 v218, v162, v163
	v_cvt_pk_bf16_f32 v219, v164, v165
	v_cvt_pk_bf16_f32 v220, v158, v159
	v_cvt_pk_bf16_f32 v221, v160, v161
	s_nop 0
	v_add_f32_e32 v233, v190, v191
	v_lshlrev_b32_e32 v190, 1, v0
	global_store_dwordx4 v190, v[218:221], s[12:13]

; #define PG8_GAS __attribute__((address_space(1)))
; #define PG8_PACK8(y0, y1) (u32x4){cvt_pk_bf16((y0)[0], (y0)[1]), cvt_pk_bf16((y0)[2], (y0)[3]), cvt_pk_bf16((y1)[0], (y1)[1]), cvt_pk_bf16((y1)[2], (y1)[3])}
;     __device__ __forceinline__ void operator()(const f32x4 (&acc)[2][2][4][2], const Unit& u, int ui, int wr, int wc, int fr, int fq) const {
;     ...
;                 for (int bj = 0; bj < 2; ++bj) {
;                     const unsigned off = row * 1024u + col0 + bj * HALF;
;                     const u32x4 x4 = xw[ai][m][bj];
;                     f32x4 o0, o1;
;                     o0[0] = __builtin_bit_cast(float, x4[0] << 16) + acc[ai][bj][m][0][0]; o0[1] = __builtin_bit_cast(float, x4[0] & 0xffff0000u) + acc[ai][bj][m][0][1];
;                     o0[2] = __builtin_bit_cast(float, x4[1] << 16) + acc[ai][bj][m][0][2]; o0[3] = __builtin_bit_cast(float, x4[1] & 0xffff0000u) + acc[ai][bj][m][0][3];
;                     o1[0] = __builtin_bit_cast(float, x4[2] << 16) + acc[ai][bj][m][1][0]; o1[1] = __builtin_bit_cast(float, x4[2] & 0xffff0000u) + acc[ai][bj][m][1][1];
;                     o1[2] = __builtin_bit_cast(float, x4[3] << 16) + acc[ai][bj][m][1][2]; o1[3] = __builtin_bit_cast(float, x4[3] & 0xffff0000u) + acc[ai][bj][m][1][3];
;                     if (last) { __builtin_nontemporal_store(o0, (PG8_GAS f32x4*)((PG8_GAS float*)out + (size_t)off)); __builtin_nontemporal_store(o1, (PG8_GAS f32x4*)((PG8_GAS float*)out + (size_t)off + 4)); }
;                     else {
;                         const f32x4 q4 = o0 * o0 + o1 * o1; ss += (q4[0] + q4[1]) + (q4[2] + q4[3]);
;                         *(PG8_GAS u32x4*)((PG8_GAS unsigned char*)ws + E_XB + (size_t)(off * 2u)) = PG8_PACK8(o0, o1);
.LBB0_425:
	s_nop 1
	s_waitcnt vmcnt(15)
	v_lshlrev_b32_e32 v158, 16, v186
	v_and_b32_e32 v159, 0xffff0000, v186
	v_pk_add_f32 v[146:147], v[146:147], v[158:159]
	v_lshlrev_b32_e32 v158, 16, v187
	v_and_b32_e32 v159, 0xffff0000, v187
	v_pk_add_f32 v[148:149], v[148:149], v[158:159]
	v_lshlrev_b32_e32 v158, 16, v188
	v_and_b32_e32 v159, 0xffff0000, v188
	v_pk_add_f32 v[138:139], v[138:139], v[158:159]
	v_lshlrev_b32_e32 v158, 16, v189
	v_and_b32_e32 v159, 0xffff0000, v189
	v_pk_add_f32 v[140:141], v[140:141], v[158:159]
	v_cndmask_b32_e64 v158, 0, 1, s[8:9]
	v_cmp_ne_u32_e64 s[0:1], 1, v158
	s_andn2_b64 vcc, exec, s[8:9]
	s_mov_b64 s[24:25], -1
	s_cbranch_vccnz .LBB0_427
	v_pk_mul_f32 v[158:159], v[140:141], v[140:141]
	v_pk_mul_f32 v[160:161], v[138:139], v[138:139]
	v_pk_fma_f32 v[158:159], v[148:149], v[148:149], v[158:159]
	v_pk_fma_f32 v[160:161], v[146:147], v[146:147], v[160:161]
	s_mov_b64 s[24:25], 0
	v_pk_mov_b32 v[162:163], v[160:161], v[158:159] op_sel:[1,0]
	v_mov_b32_e32 v161, v159
	v_pk_add_f32 v[158:159], v[162:163], v[160:161]
	v_cvt_pk_bf16_f32 v160, v146, v147
	v_cvt_pk_bf16_f32 v161, v148, v149
	v_cvt_pk_bf16_f32 v162, v138, v139
	v_cvt_pk_bf16_f32 v163, v140, v141
	s_nop 0
	v_add_f32_e32 v158, v158, v159
	v_mov_b32_e32 v159, 0x100
	v_add_f32_e32 v158, v158, v233
	v_lshl_or_b32 v159, v0, 1, v159
	global_store_dwordx4 v159, v[160:163], s[12:13]

; #define PG8_GAS __attribute__((address_space(1)))
; #define PG8_PACK8(y0, y1) (u32x4){cvt_pk_bf16((y0)[0], (y0)[1]), cvt_pk_bf16((y0)[2], (y0)[3]), cvt_pk_bf16((y1)[0], (y1)[1]), cvt_pk_bf16((y1)[2], (y1)[3])}
;     __device__ __forceinline__ void operator()(const f32x4 (&acc)[2][2][4][2], const Unit& u, int ui, int wr, int wc, int fr, int fq) const {
;     ...
;                 for (int bj = 0; bj < 2; ++bj) {
;                     const unsigned off = row * 1024u + col0 + bj * HALF;
;                     const u32x4 x4 = xw[ai][m][bj];
;                     f32x4 o0, o1;
;                     o0[0] = __builtin_bit_cast(float, x4[0] << 16) + acc[ai][bj][m][0][0]; o0[1] = __builtin_bit_cast(float, x4[0] & 0xffff0000u) + acc[ai][bj][m][0][1];
;                     o0[2] = __builtin_bit_cast(float, x4[1] << 16) + acc[ai][bj][m][0][2]; o0[3] = __builtin_bit_cast(float, x4[1] & 0xffff0000u) + acc[ai][bj][m][0][3];
;                     o1[0] = __builtin_bit_cast(float, x4[2] << 16) + acc[ai][bj][m][1][0]; o1[1] = __builtin_bit_cast(float, x4[2] & 0xffff0000u) + acc[ai][bj][m][1][1];
;                     o1[2] = __builtin_bit_cast(float, x4[3] << 16) + acc[ai][bj][m][1][2]; o1[3] = __builtin_bit_cast(float, x4[3] & 0xffff0000u) + acc[ai][bj][m][1][3];
;                     if (last) { __builtin_nontemporal_store(o0, (PG8_GAS f32x4*)((PG8_GAS float*)out + (size_t)off)); __builtin_nontemporal_store(o1, (PG8_GAS f32x4*)((PG8_GAS float*)out + (size_t)off + 4)); }
;                     else {
;                         const f32x4 q4 = o0 * o0 + o1 * o1; ss += (q4[0] + q4[1]) + (q4[2] + q4[3]);
;                         *(PG8_GAS u32x4*)((PG8_GAS unsigned char*)ws + E_XB + (size_t)(off * 2u)) = PG8_PACK8(o0, o1);
.LBB0_429:
	s_waitcnt vmcnt(15)
	v_lshlrev_b32_e32 v140, 16, v182
	v_and_b32_e32 v141, 0xffff0000, v182
	v_pk_add_f32 v[134:135], v[134:135], v[140:141]
	v_lshlrev_b32_e32 v140, 16, v183
	v_and_b32_e32 v141, 0xffff0000, v183
	v_pk_add_f32 v[136:137], v[136:137], v[140:141]
	v_lshlrev_b32_e32 v140, 16, v184
	v_and_b32_e32 v141, 0xffff0000, v184
	v_pk_add_f32 v[130:131], v[130:131], v[140:141]
	v_lshlrev_b32_e32 v140, 16, v185
	v_and_b32_e32 v141, 0xffff0000, v185
	v_add_u32_e32 v138, 0x4000, v0
	v_pk_add_f32 v[132:133], v[132:133], v[140:141]
	s_and_b64 vcc, exec, s[0:1]
	s_mov_b64 s[24:25], -1
	s_cbranch_vccnz .LBB0_431
	v_pk_mul_f32 v[140:141], v[132:133], v[132:133]
	v_pk_mul_f32 v[146:147], v[130:131], v[130:131]
	v_pk_fma_f32 v[140:141], v[136:137], v[136:137], v[140:141]
	v_pk_fma_f32 v[146:147], v[134:135], v[134:135], v[146:147]
	s_mov_b64 s[24:25], 0
	v_pk_mov_b32 v[148:149], v[146:147], v[140:141] op_sel:[1,0]
	v_mov_b32_e32 v147, v141
	v_pk_add_f32 v[140:141], v[148:149], v[146:147]
	v_cvt_pk_bf16_f32 v146, v134, v135
	v_cvt_pk_bf16_f32 v147, v136, v137
	v_cvt_pk_bf16_f32 v148, v130, v131
	v_cvt_pk_bf16_f32 v149, v132, v133
	s_nop 0
	v_add_f32_e32 v139, v140, v141
	v_lshlrev_b32_e32 v140, 1, v138
	global_store_dwordx4 v140, v[146:149], s[12:13]

; #define PG8_GAS __attribute__((address_space(1)))
; #define PG8_PACK8(y0, y1) (u32x4){cvt_pk_bf16((y0)[0], (y0)[1]), cvt_pk_bf16((y0)[2], (y0)[3]), cvt_pk_bf16((y1)[0], (y1)[1]), cvt_pk_bf16((y1)[2], (y1)[3])}
;     __device__ __forceinline__ void operator()(const f32x4 (&acc)[2][2][4][2], const Unit& u, int ui, int wr, int wc, int fr, int fq) const {
;     ...
;                 for (int bj = 0; bj < 2; ++bj) {
;                     const unsigned off = row * 1024u + col0 + bj * HALF;
;                     const u32x4 x4 = xw[ai][m][bj];
;                     f32x4 o0, o1;
;                     o0[0] = __builtin_bit_cast(float, x4[0] << 16) + acc[ai][bj][m][0][0]; o0[1] = __builtin_bit_cast(float, x4[0] & 0xffff0000u) + acc[ai][bj][m][0][1];
;                     o0[2] = __builtin_bit_cast(float, x4[1] << 16) + acc[ai][bj][m][0][2]; o0[3] = __builtin_bit_cast(float, x4[1] & 0xffff0000u) + acc[ai][bj][m][0][3];
;                     o1[0] = __builtin_bit_cast(float, x4[2] << 16) + acc[ai][bj][m][1][0]; o1[1] = __builtin_bit_cast(float, x4[2] & 0xffff0000u) + acc[ai][bj][m][1][1];
;                     o1[2] = __builtin_bit_cast(float, x4[3] << 16) + acc[ai][bj][m][1][2]; o1[3] = __builtin_bit_cast(float, x4[3] & 0xffff0000u) + acc[ai][bj][m][1][3];
;                     if (last) { __builtin_nontemporal_store(o0, (PG8_GAS f32x4*)((PG8_GAS float*)out + (size_t)off)); __builtin_nontemporal_store(o1, (PG8_GAS f32x4*)((PG8_GAS float*)out + (size_t)off + 4)); }
;                     else {
;                         const f32x4 q4 = o0 * o0 + o1 * o1; ss += (q4[0] + q4[1]) + (q4[2] + q4[3]);
;                         *(PG8_GAS u32x4*)((PG8_GAS unsigned char*)ws + E_XB + (size_t)(off * 2u)) = PG8_PACK8(o0, o1);
.LBB0_433:
	s_waitcnt vmcnt(15)
	v_lshlrev_b32_e32 v132, 16, v178
	v_and_b32_e32 v133, 0xffff0000, v178
	v_pk_add_f32 v[118:119], v[118:119], v[132:133]
	v_lshlrev_b32_e32 v132, 16, v179
	v_and_b32_e32 v133, 0xffff0000, v179
	v_pk_add_f32 v[120:121], v[120:121], v[132:133]
	v_lshlrev_b32_e32 v132, 16, v180
	v_and_b32_e32 v133, 0xffff0000, v180
	v_pk_add_f32 v[114:115], v[114:115], v[132:133]
	v_lshlrev_b32_e32 v132, 16, v181
	v_and_b32_e32 v133, 0xffff0000, v181
	v_add_u32_e32 v130, 0x4080, v0
	v_pk_add_f32 v[116:117], v[116:117], v[132:133]
	s_and_b64 vcc, exec, s[0:1]
	s_mov_b64 s[24:25], -1
	s_cbranch_vccnz .LBB0_435
	v_pk_mul_f32 v[132:133], v[116:117], v[116:117]
	v_pk_mul_f32 v[134:135], v[114:115], v[114:115]
	v_pk_fma_f32 v[132:133], v[120:121], v[120:121], v[132:133]
	v_pk_fma_f32 v[134:135], v[118:119], v[118:119], v[134:135]
	s_mov_b64 s[24:25], 0
	v_pk_mov_b32 v[136:137], v[134:135], v[132:133] op_sel:[1,0]
	v_mov_b32_e32 v135, v133
	v_pk_add_f32 v[132:133], v[136:137], v[134:135]
	v_lshlrev_b32_e32 v136, 1, v130
	v_add_f32_e32 v131, v132, v133
	v_add_f32_e32 v131, v131, v139
	v_cvt_pk_bf16_f32 v132, v118, v119
	v_cvt_pk_bf16_f32 v133, v120, v121
	v_cvt_pk_bf16_f32 v134, v114, v115
	v_cvt_pk_bf16_f32 v135, v116, v117
	global_store_dwordx4 v136, v[132:135], s[12:13]

; #define PG8_GAS __attribute__((address_space(1)))
; #define PG8_PACK8(y0, y1) (u32x4){cvt_pk_bf16((y0)[0], (y0)[1]), cvt_pk_bf16((y0)[2], (y0)[3]), cvt_pk_bf16((y1)[0], (y1)[1]), cvt_pk_bf16((y1)[2], (y1)[3])}
;     __device__ __forceinline__ void operator()(const f32x4 (&acc)[2][2][4][2], const Unit& u, int ui, int wr, int wc, int fr, int fq) const {
;     ...
;                 for (int bj = 0; bj < 2; ++bj) {
;                     const unsigned off = row * 1024u + col0 + bj * HALF;
;                     const u32x4 x4 = xw[ai][m][bj];
;                     f32x4 o0, o1;
;                     o0[0] = __builtin_bit_cast(float, x4[0] << 16) + acc[ai][bj][m][0][0]; o0[1] = __builtin_bit_cast(float, x4[0] & 0xffff0000u) + acc[ai][bj][m][0][1];
;                     o0[2] = __builtin_bit_cast(float, x4[1] << 16) + acc[ai][bj][m][0][2]; o0[3] = __builtin_bit_cast(float, x4[1] & 0xffff0000u) + acc[ai][bj][m][0][3];
;                     o1[0] = __builtin_bit_cast(float, x4[2] << 16) + acc[ai][bj][m][1][0]; o1[1] = __builtin_bit_cast(float, x4[2] & 0xffff0000u) + acc[ai][bj][m][1][1];
;                     o1[2] = __builtin_bit_cast(float, x4[3] << 16) + acc[ai][bj][m][1][2]; o1[3] = __builtin_bit_cast(float, x4[3] & 0xffff0000u) + acc[ai][bj][m][1][3];
;                     if (last) { __builtin_nontemporal_store(o0, (PG8_GAS f32x4*)((PG8_GAS float*)out + (size_t)off)); __builtin_nontemporal_store(o1, (PG8_GAS f32x4*)((PG8_GAS float*)out + (size_t)off + 4)); }
;                     else {
;                         const f32x4 q4 = o0 * o0 + o1 * o1; ss += (q4[0] + q4[1]) + (q4[2] + q4[3]);
;                         *(PG8_GAS u32x4*)((PG8_GAS unsigned char*)ws + E_XB + (size_t)(off * 2u)) = PG8_PACK8(o0, o1);
.LBB0_437:
	s_waitcnt vmcnt(15)
	v_lshlrev_b32_e32 v116, 16, v174
	v_and_b32_e32 v117, 0xffff0000, v174
	v_pk_add_f32 v[110:111], v[110:111], v[116:117]
	v_lshlrev_b32_e32 v116, 16, v175
	v_and_b32_e32 v117, 0xffff0000, v175
	v_pk_add_f32 v[112:113], v[112:113], v[116:117]
	v_lshlrev_b32_e32 v116, 16, v176
	v_and_b32_e32 v117, 0xffff0000, v176
	v_pk_add_f32 v[102:103], v[102:103], v[116:117]
	v_lshlrev_b32_e32 v116, 16, v177
	v_and_b32_e32 v117, 0xffff0000, v177
	v_add_u32_e32 v114, 0x8000, v0
	v_pk_add_f32 v[104:105], v[104:105], v[116:117]
	s_and_b64 vcc, exec, s[0:1]
	s_mov_b64 s[24:25], -1
	s_cbranch_vccnz .LBB0_439
	v_pk_mul_f32 v[116:117], v[104:105], v[104:105]
	v_pk_mul_f32 v[118:119], v[102:103], v[102:103]
	v_pk_fma_f32 v[116:117], v[112:113], v[112:113], v[116:117]
	v_pk_fma_f32 v[118:119], v[110:111], v[110:111], v[118:119]
	s_mov_b64 s[24:25], 0
	v_pk_mov_b32 v[120:121], v[118:119], v[116:117] op_sel:[1,0]
	v_mov_b32_e32 v119, v117
	v_pk_add_f32 v[116:117], v[120:121], v[118:119]
	v_lshlrev_b32_e32 v120, 1, v114
	v_add_f32_e32 v115, v116, v117
	v_cvt_pk_bf16_f32 v116, v110, v111
	v_cvt_pk_bf16_f32 v117, v112, v113
	v_cvt_pk_bf16_f32 v118, v102, v103
	v_cvt_pk_bf16_f32 v119, v104, v105
	global_store_dwordx4 v120, v[116:119], s[12:13]

; #define PG8_GAS __attribute__((address_space(1)))
; #define PG8_PACK8(y0, y1) (u32x4){cvt_pk_bf16((y0)[0], (y0)[1]), cvt_pk_bf16((y0)[2], (y0)[3]), cvt_pk_bf16((y1)[0], (y1)[1]), cvt_pk_bf16((y1)[2], (y1)[3])}
;     __device__ __forceinline__ void operator()(const f32x4 (&acc)[2][2][4][2], const Unit& u, int ui, int wr, int wc, int fr, int fq) const {
;     ...
;                 for (int bj = 0; bj < 2; ++bj) {
;                     const unsigned off = row * 1024u + col0 + bj * HALF;
;                     const u32x4 x4 = xw[ai][m][bj];
;                     f32x4 o0, o1;
;                     o0[0] = __builtin_bit_cast(float, x4[0] << 16) + acc[ai][bj][m][0][0]; o0[1] = __builtin_bit_cast(float, x4[0] & 0xffff0000u) + acc[ai][bj][m][0][1];
;                     o0[2] = __builtin_bit_cast(float, x4[1] << 16) + acc[ai][bj][m][0][2]; o0[3] = __builtin_bit_cast(float, x4[1] & 0xffff0000u) + acc[ai][bj][m][0][3];
;                     o1[0] = __builtin_bit_cast(float, x4[2] << 16) + acc[ai][bj][m][1][0]; o1[1] = __builtin_bit_cast(float, x4[2] & 0xffff0000u) + acc[ai][bj][m][1][1];
;                     o1[2] = __builtin_bit_cast(float, x4[3] << 16) + acc[ai][bj][m][1][2]; o1[3] = __builtin_bit_cast(float, x4[3] & 0xffff0000u) + acc[ai][bj][m][1][3];
;                     if (last) { __builtin_nontemporal_store(o0, (PG8_GAS f32x4*)((PG8_GAS float*)out + (size_t)off)); __builtin_nontemporal_store(o1, (PG8_GAS f32x4*)((PG8_GAS float*)out + (size_t)off + 4)); }
;                     else {
;                         const f32x4 q4 = o0 * o0 + o1 * o1; ss += (q4[0] + q4[1]) + (q4[2] + q4[3]);
;                         *(PG8_GAS u32x4*)((PG8_GAS unsigned char*)ws + E_XB + (size_t)(off * 2u)) = PG8_PACK8(o0, o1);
.LBB0_441:
	s_waitcnt vmcnt(15)
	v_lshlrev_b32_e32 v104, 16, v170
	v_and_b32_e32 v105, 0xffff0000, v170
	v_pk_add_f32 v[94:95], v[94:95], v[104:105]
	v_lshlrev_b32_e32 v104, 16, v171
	v_and_b32_e32 v105, 0xffff0000, v171
	v_pk_add_f32 v[96:97], v[96:97], v[104:105]
	v_lshlrev_b32_e32 v104, 16, v172
	v_and_b32_e32 v105, 0xffff0000, v172
	v_pk_add_f32 v[90:91], v[90:91], v[104:105]
	v_lshlrev_b32_e32 v104, 16, v173
	v_and_b32_e32 v105, 0xffff0000, v173
	v_add_u32_e32 v102, 0x8080, v0
	v_pk_add_f32 v[92:93], v[92:93], v[104:105]
	s_and_b64 vcc, exec, s[0:1]
	s_mov_b64 s[24:25], -1
	s_cbranch_vccnz .LBB0_443
	v_pk_mul_f32 v[104:105], v[92:93], v[92:93]
	v_pk_mul_f32 v[110:111], v[90:91], v[90:91]
	v_pk_fma_f32 v[104:105], v[96:97], v[96:97], v[104:105]
	v_pk_fma_f32 v[110:111], v[94:95], v[94:95], v[110:111]
	s_mov_b64 s[24:25], 0
	v_pk_mov_b32 v[112:113], v[110:111], v[104:105] op_sel:[1,0]
	v_mov_b32_e32 v111, v105
	v_pk_add_f32 v[104:105], v[112:113], v[110:111]
	v_cvt_pk_bf16_f32 v110, v94, v95
	v_cvt_pk_bf16_f32 v111, v96, v97
	v_cvt_pk_bf16_f32 v112, v90, v91
	v_cvt_pk_bf16_f32 v113, v92, v93
	s_nop 0
	v_add_f32_e32 v103, v104, v105
	v_add_f32_e32 v103, v103, v115
	v_lshlrev_b32_e32 v104, 1, v102
	global_store_dwordx4 v104, v[110:113], s[12:13]

; #define PG8_GAS __attribute__((address_space(1)))
; #define PG8_PACK8(y0, y1) (u32x4){cvt_pk_bf16((y0)[0], (y0)[1]), cvt_pk_bf16((y0)[2], (y0)[3]), cvt_pk_bf16((y1)[0], (y1)[1]), cvt_pk_bf16((y1)[2], (y1)[3])}
;     __device__ __forceinline__ void operator()(const f32x4 (&acc)[2][2][4][2], const Unit& u, int ui, int wr, int wc, int fr, int fq) const {
;     ...
;                 for (int bj = 0; bj < 2; ++bj) {
;                     const unsigned off = row * 1024u + col0 + bj * HALF;
;                     const u32x4 x4 = xw[ai][m][bj];
;                     f32x4 o0, o1;
;                     o0[0] = __builtin_bit_cast(float, x4[0] << 16) + acc[ai][bj][m][0][0]; o0[1] = __builtin_bit_cast(float, x4[0] & 0xffff0000u) + acc[ai][bj][m][0][1];
;                     o0[2] = __builtin_bit_cast(float, x4[1] << 16) + acc[ai][bj][m][0][2]; o0[3] = __builtin_bit_cast(float, x4[1] & 0xffff0000u) + acc[ai][bj][m][0][3];
;                     o1[0] = __builtin_bit_cast(float, x4[2] << 16) + acc[ai][bj][m][1][0]; o1[1] = __builtin_bit_cast(float, x4[2] & 0xffff0000u) + acc[ai][bj][m][1][1];
;                     o1[2] = __builtin_bit_cast(float, x4[3] << 16) + acc[ai][bj][m][1][2]; o1[3] = __builtin_bit_cast(float, x4[3] & 0xffff0000u) + acc[ai][bj][m][1][3];
;                     if (last) { __builtin_nontemporal_store(o0, (PG8_GAS f32x4*)((PG8_GAS float*)out + (size_t)off)); __builtin_nontemporal_store(o1, (PG8_GAS f32x4*)((PG8_GAS float*)out + (size_t)off + 4)); }
;                     else {
;                         const f32x4 q4 = o0 * o0 + o1 * o1; ss += (q4[0] + q4[1]) + (q4[2] + q4[3]);
;                         *(PG8_GAS u32x4*)((PG8_GAS unsigned char*)ws + E_XB + (size_t)(off * 2u)) = PG8_PACK8(o0, o1);
.LBB0_445:
	s_waitcnt vmcnt(15)
	v_lshlrev_b32_e32 v92, 16, v166
	v_and_b32_e32 v93, 0xffff0000, v166
	v_pk_add_f32 v[82:83], v[82:83], v[92:93]
	v_lshlrev_b32_e32 v92, 16, v167
	v_and_b32_e32 v93, 0xffff0000, v167
	v_pk_add_f32 v[84:85], v[84:85], v[92:93]
	v_lshlrev_b32_e32 v92, 16, v168
	v_and_b32_e32 v93, 0xffff0000, v168
	v_pk_add_f32 v[78:79], v[78:79], v[92:93]
	v_lshlrev_b32_e32 v92, 16, v169
	v_and_b32_e32 v93, 0xffff0000, v169
	v_add_u32_e32 v90, 0xc000, v0
	v_pk_add_f32 v[80:81], v[80:81], v[92:93]
	s_and_b64 vcc, exec, s[0:1]
	s_mov_b64 s[24:25], -1
	s_cbranch_vccnz .LBB0_447
	v_pk_mul_f32 v[92:93], v[80:81], v[80:81]
	v_pk_mul_f32 v[94:95], v[78:79], v[78:79]
	v_pk_fma_f32 v[92:93], v[84:85], v[84:85], v[92:93]
	v_pk_fma_f32 v[94:95], v[82:83], v[82:83], v[94:95]
	s_mov_b64 s[24:25], 0
	v_pk_mov_b32 v[96:97], v[94:95], v[92:93] op_sel:[1,0]
	v_mov_b32_e32 v95, v93
	v_pk_add_f32 v[92:93], v[96:97], v[94:95]
	v_lshlrev_b32_e32 v96, 1, v90
	v_add_f32_e32 v91, v92, v93
	v_cvt_pk_bf16_f32 v92, v82, v83
	v_cvt_pk_bf16_f32 v93, v84, v85
	v_cvt_pk_bf16_f32 v94, v78, v79
	v_cvt_pk_bf16_f32 v95, v80, v81
	global_store_dwordx4 v96, v[92:95], s[12:13]

; #define PG8_GAS __attribute__((address_space(1)))
; #define PG8_PACK8(y0, y1) (u32x4){cvt_pk_bf16((y0)[0], (y0)[1]), cvt_pk_bf16((y0)[2], (y0)[3]), cvt_pk_bf16((y1)[0], (y1)[1]), cvt_pk_bf16((y1)[2], (y1)[3])}
;     __device__ __forceinline__ void operator()(const f32x4 (&acc)[2][2][4][2], const Unit& u, int ui, int wr, int wc, int fr, int fq) const {
;     ...
;                 for (int bj = 0; bj < 2; ++bj) {
;                     const unsigned off = row * 1024u + col0 + bj * HALF;
;                     const u32x4 x4 = xw[ai][m][bj];
;                     f32x4 o0, o1;
;                     o0[0] = __builtin_bit_cast(float, x4[0] << 16) + acc[ai][bj][m][0][0]; o0[1] = __builtin_bit_cast(float, x4[0] & 0xffff0000u) + acc[ai][bj][m][0][1];
;                     o0[2] = __builtin_bit_cast(float, x4[1] << 16) + acc[ai][bj][m][0][2]; o0[3] = __builtin_bit_cast(float, x4[1] & 0xffff0000u) + acc[ai][bj][m][0][3];
;                     o1[0] = __builtin_bit_cast(float, x4[2] << 16) + acc[ai][bj][m][1][0]; o1[1] = __builtin_bit_cast(float, x4[2] & 0xffff0000u) + acc[ai][bj][m][1][1];
;                     o1[2] = __builtin_bit_cast(float, x4[3] << 16) + acc[ai][bj][m][1][2]; o1[3] = __builtin_bit_cast(float, x4[3] & 0xffff0000u) + acc[ai][bj][m][1][3];
;                     if (last) { __builtin_nontemporal_store(o0, (PG8_GAS f32x4*)((PG8_GAS float*)out + (size_t)off)); __builtin_nontemporal_store(o1, (PG8_GAS f32x4*)((PG8_GAS float*)out + (size_t)off + 4)); }
;                     else {
;                         const f32x4 q4 = o0 * o0 + o1 * o1; ss += (q4[0] + q4[1]) + (q4[2] + q4[3]);
;                         *(PG8_GAS u32x4*)((PG8_GAS unsigned char*)ws + E_XB + (size_t)(off * 2u)) = PG8_PACK8(o0, o1);
.LBB0_449:
	s_waitcnt vmcnt(15)
	v_lshlrev_b32_e32 v80, 16, v154
	v_and_b32_e32 v81, 0xffff0000, v154
	v_pk_add_f32 v[70:71], v[70:71], v[80:81]
	v_lshlrev_b32_e32 v80, 16, v155
	v_and_b32_e32 v81, 0xffff0000, v155
	v_pk_add_f32 v[72:73], v[72:73], v[80:81]
	v_lshlrev_b32_e32 v80, 16, v156
	v_and_b32_e32 v81, 0xffff0000, v156
	v_pk_add_f32 v[66:67], v[66:67], v[80:81]
	v_lshlrev_b32_e32 v80, 16, v157
	v_and_b32_e32 v81, 0xffff0000, v157
	v_add_u32_e32 v78, 0xc080, v0
	v_pk_add_f32 v[68:69], v[68:69], v[80:81]
	s_and_b64 vcc, exec, s[0:1]
	s_mov_b64 s[24:25], -1
	s_cbranch_vccnz .LBB0_451
	v_pk_mul_f32 v[80:81], v[68:69], v[68:69]
	v_pk_mul_f32 v[82:83], v[66:67], v[66:67]
	v_pk_fma_f32 v[80:81], v[72:73], v[72:73], v[80:81]
	v_pk_fma_f32 v[82:83], v[70:71], v[70:71], v[82:83]
	s_mov_b64 s[24:25], 0
	v_pk_mov_b32 v[84:85], v[82:83], v[80:81] op_sel:[1,0]
	v_mov_b32_e32 v83, v81
	v_pk_add_f32 v[80:81], v[84:85], v[82:83]
	v_lshlrev_b32_e32 v84, 1, v78
	v_add_f32_e32 v79, v80, v81
	v_add_f32_e32 v79, v79, v91
	v_cvt_pk_bf16_f32 v80, v70, v71
	v_cvt_pk_bf16_f32 v81, v72, v73
	v_cvt_pk_bf16_f32 v82, v66, v67
	v_cvt_pk_bf16_f32 v83, v68, v69
	global_store_dwordx4 v84, v[80:83], s[12:13]

; #define PG8_GAS __attribute__((address_space(1)))
; #define PG8_PACK8(y0, y1) (u32x4){cvt_pk_bf16((y0)[0], (y0)[1]), cvt_pk_bf16((y0)[2], (y0)[3]), cvt_pk_bf16((y1)[0], (y1)[1]), cvt_pk_bf16((y1)[2], (y1)[3])}
;     __device__ __forceinline__ void operator()(const f32x4 (&acc)[2][2][4][2], const Unit& u, int ui, int wr, int wc, int fr, int fq) const {
;     ...
;                 for (int bj = 0; bj < 2; ++bj) {
;                     const unsigned off = row * 1024u + col0 + bj * HALF;
;                     const u32x4 x4 = xw[ai][m][bj];
;                     f32x4 o0, o1;
;                     o0[0] = __builtin_bit_cast(float, x4[0] << 16) + acc[ai][bj][m][0][0]; o0[1] = __builtin_bit_cast(float, x4[0] & 0xffff0000u) + acc[ai][bj][m][0][1];
;                     o0[2] = __builtin_bit_cast(float, x4[1] << 16) + acc[ai][bj][m][0][2]; o0[3] = __builtin_bit_cast(float, x4[1] & 0xffff0000u) + acc[ai][bj][m][0][3];
;                     o1[0] = __builtin_bit_cast(float, x4[2] << 16) + acc[ai][bj][m][1][0]; o1[1] = __builtin_bit_cast(float, x4[2] & 0xffff0000u) + acc[ai][bj][m][1][1];
;                     o1[2] = __builtin_bit_cast(float, x4[3] << 16) + acc[ai][bj][m][1][2]; o1[3] = __builtin_bit_cast(float, x4[3] & 0xffff0000u) + acc[ai][bj][m][1][3];
;                     if (last) { __builtin_nontemporal_store(o0, (PG8_GAS f32x4*)((PG8_GAS float*)out + (size_t)off)); __builtin_nontemporal_store(o1, (PG8_GAS f32x4*)((PG8_GAS float*)out + (size_t)off + 4)); }
;                     else {
;                         const f32x4 q4 = o0 * o0 + o1 * o1; ss += (q4[0] + q4[1]) + (q4[2] + q4[3]);
;                         *(PG8_GAS u32x4*)((PG8_GAS unsigned char*)ws + E_XB + (size_t)(off * 2u)) = PG8_PACK8(o0, o1);
.LBB0_453:
	s_waitcnt vmcnt(15)
	v_lshlrev_b32_e32 v68, 16, v150
	v_and_b32_e32 v69, 0xffff0000, v150
	v_pk_add_f32 v[62:63], v[62:63], v[68:69]
	v_lshlrev_b32_e32 v68, 16, v151
	v_and_b32_e32 v69, 0xffff0000, v151
	v_pk_add_f32 v[64:65], v[64:65], v[68:69]
	v_lshlrev_b32_e32 v68, 16, v152
	v_and_b32_e32 v69, 0xffff0000, v152
	v_pk_add_f32 v[58:59], v[58:59], v[68:69]
	v_lshlrev_b32_e32 v68, 16, v153
	v_and_b32_e32 v69, 0xffff0000, v153
	v_add_u32_e32 v66, 0x20000, v0
	v_pk_add_f32 v[60:61], v[60:61], v[68:69]
	s_and_b64 vcc, exec, s[0:1]
	s_mov_b64 s[24:25], -1
	s_cbranch_vccnz .LBB0_455
	v_pk_mul_f32 v[68:69], v[60:61], v[60:61]
	v_pk_mul_f32 v[70:71], v[58:59], v[58:59]
	v_pk_fma_f32 v[68:69], v[64:65], v[64:65], v[68:69]
	v_pk_fma_f32 v[70:71], v[62:63], v[62:63], v[70:71]
	s_mov_b64 s[24:25], 0
	v_pk_mov_b32 v[72:73], v[70:71], v[68:69] op_sel:[1,0]
	v_mov_b32_e32 v71, v69
	v_pk_add_f32 v[68:69], v[72:73], v[70:71]
	v_lshlrev_b32_e32 v72, 1, v66
	v_add_f32_e32 v67, v68, v69
	v_cvt_pk_bf16_f32 v68, v62, v63
	v_cvt_pk_bf16_f32 v69, v64, v65
	v_cvt_pk_bf16_f32 v70, v58, v59
	v_cvt_pk_bf16_f32 v71, v60, v61
	global_store_dwordx4 v72, v[68:71], s[12:13]

; #define PG8_GAS __attribute__((address_space(1)))
; #define PG8_PACK8(y0, y1) (u32x4){cvt_pk_bf16((y0)[0], (y0)[1]), cvt_pk_bf16((y0)[2], (y0)[3]), cvt_pk_bf16((y1)[0], (y1)[1]), cvt_pk_bf16((y1)[2], (y1)[3])}
;     __device__ __forceinline__ void operator()(const f32x4 (&acc)[2][2][4][2], const Unit& u, int ui, int wr, int wc, int fr, int fq) const {
;     ...
;                 for (int bj = 0; bj < 2; ++bj) {
;                     const unsigned off = row * 1024u + col0 + bj * HALF;
;                     const u32x4 x4 = xw[ai][m][bj];
;                     f32x4 o0, o1;
;                     o0[0] = __builtin_bit_cast(float, x4[0] << 16) + acc[ai][bj][m][0][0]; o0[1] = __builtin_bit_cast(float, x4[0] & 0xffff0000u) + acc[ai][bj][m][0][1];
;                     o0[2] = __builtin_bit_cast(float, x4[1] << 16) + acc[ai][bj][m][0][2]; o0[3] = __builtin_bit_cast(float, x4[1] & 0xffff0000u) + acc[ai][bj][m][0][3];
;                     o1[0] = __builtin_bit_cast(float, x4[2] << 16) + acc[ai][bj][m][1][0]; o1[1] = __builtin_bit_cast(float, x4[2] & 0xffff0000u) + acc[ai][bj][m][1][1];
;                     o1[2] = __builtin_bit_cast(float, x4[3] << 16) + acc[ai][bj][m][1][2]; o1[3] = __builtin_bit_cast(float, x4[3] & 0xffff0000u) + acc[ai][bj][m][1][3];
;                     if (last) { __builtin_nontemporal_store(o0, (PG8_GAS f32x4*)((PG8_GAS float*)out + (size_t)off)); __builtin_nontemporal_store(o1, (PG8_GAS f32x4*)((PG8_GAS float*)out + (size_t)off + 4)); }
;                     else {
;                         const f32x4 q4 = o0 * o0 + o1 * o1; ss += (q4[0] + q4[1]) + (q4[2] + q4[3]);
;                         *(PG8_GAS u32x4*)((PG8_GAS unsigned char*)ws + E_XB + (size_t)(off * 2u)) = PG8_PACK8(o0, o1);
.LBB0_457:
	s_waitcnt vmcnt(15)
	v_lshlrev_b32_e32 v60, 16, v142
	v_and_b32_e32 v61, 0xffff0000, v142
	v_pk_add_f32 v[54:55], v[54:55], v[60:61]
	v_lshlrev_b32_e32 v60, 16, v143
	v_and_b32_e32 v61, 0xffff0000, v143
	v_pk_add_f32 v[56:57], v[56:57], v[60:61]
	v_lshlrev_b32_e32 v60, 16, v144
	v_and_b32_e32 v61, 0xffff0000, v144
	v_pk_add_f32 v[50:51], v[50:51], v[60:61]
	v_lshlrev_b32_e32 v60, 16, v145
	v_and_b32_e32 v61, 0xffff0000, v145
	v_add_u32_e32 v58, 0x20080, v0
	v_pk_add_f32 v[52:53], v[52:53], v[60:61]
	s_and_b64 vcc, exec, s[0:1]
	s_mov_b64 s[24:25], -1
	s_cbranch_vccnz .LBB0_459
	v_pk_mul_f32 v[60:61], v[52:53], v[52:53]
	v_pk_mul_f32 v[62:63], v[50:51], v[50:51]
	v_pk_fma_f32 v[60:61], v[56:57], v[56:57], v[60:61]
	v_pk_fma_f32 v[62:63], v[54:55], v[54:55], v[62:63]
	s_mov_b64 s[24:25], 0
	v_pk_mov_b32 v[64:65], v[62:63], v[60:61] op_sel:[1,0]
	v_mov_b32_e32 v63, v61
	v_pk_add_f32 v[60:61], v[64:65], v[62:63]
	v_lshlrev_b32_e32 v64, 1, v58
	v_add_f32_e32 v59, v60, v61
	v_add_f32_e32 v59, v59, v67
	v_cvt_pk_bf16_f32 v60, v54, v55
	v_cvt_pk_bf16_f32 v61, v56, v57
	v_cvt_pk_bf16_f32 v62, v50, v51
	v_cvt_pk_bf16_f32 v63, v52, v53
	global_store_dwordx4 v64, v[60:63], s[12:13]

; #define PG8_GAS __attribute__((address_space(1)))
; #define PG8_PACK8(y0, y1) (u32x4){cvt_pk_bf16((y0)[0], (y0)[1]), cvt_pk_bf16((y0)[2], (y0)[3]), cvt_pk_bf16((y1)[0], (y1)[1]), cvt_pk_bf16((y1)[2], (y1)[3])}
;     __device__ __forceinline__ void operator()(const f32x4 (&acc)[2][2][4][2], const Unit& u, int ui, int wr, int wc, int fr, int fq) const {
;     ...
;                 for (int bj = 0; bj < 2; ++bj) {
;                     const unsigned off = row * 1024u + col0 + bj * HALF;
;                     const u32x4 x4 = xw[ai][m][bj];
;                     f32x4 o0, o1;
;                     o0[0] = __builtin_bit_cast(float, x4[0] << 16) + acc[ai][bj][m][0][0]; o0[1] = __builtin_bit_cast(float, x4[0] & 0xffff0000u) + acc[ai][bj][m][0][1];
;                     o0[2] = __builtin_bit_cast(float, x4[1] << 16) + acc[ai][bj][m][0][2]; o0[3] = __builtin_bit_cast(float, x4[1] & 0xffff0000u) + acc[ai][bj][m][0][3];
;                     o1[0] = __builtin_bit_cast(float, x4[2] << 16) + acc[ai][bj][m][1][0]; o1[1] = __builtin_bit_cast(float, x4[2] & 0xffff0000u) + acc[ai][bj][m][1][1];
;                     o1[2] = __builtin_bit_cast(float, x4[3] << 16) + acc[ai][bj][m][1][2]; o1[3] = __builtin_bit_cast(float, x4[3] & 0xffff0000u) + acc[ai][bj][m][1][3];
;                     if (last) { __builtin_nontemporal_store(o0, (PG8_GAS f32x4*)((PG8_GAS float*)out + (size_t)off)); __builtin_nontemporal_store(o1, (PG8_GAS f32x4*)((PG8_GAS float*)out + (size_t)off + 4)); }
;                     else {
;                         const f32x4 q4 = o0 * o0 + o1 * o1; ss += (q4[0] + q4[1]) + (q4[2] + q4[3]);
;                         *(PG8_GAS u32x4*)((PG8_GAS unsigned char*)ws + E_XB + (size_t)(off * 2u)) = PG8_PACK8(o0, o1);
.LBB0_461:
	s_waitcnt vmcnt(15)
	v_lshlrev_b32_e32 v52, 16, v126
	v_and_b32_e32 v53, 0xffff0000, v126
	v_pk_add_f32 v[46:47], v[46:47], v[52:53]
	v_lshlrev_b32_e32 v52, 16, v127
	v_and_b32_e32 v53, 0xffff0000, v127
	v_pk_add_f32 v[48:49], v[48:49], v[52:53]
	v_lshlrev_b32_e32 v52, 16, v128
	v_and_b32_e32 v53, 0xffff0000, v128
	v_pk_add_f32 v[42:43], v[42:43], v[52:53]
	v_lshlrev_b32_e32 v52, 16, v129
	v_and_b32_e32 v53, 0xffff0000, v129
	v_add_u32_e32 v50, 0x24000, v0
	v_pk_add_f32 v[44:45], v[44:45], v[52:53]
	s_and_b64 vcc, exec, s[0:1]
	s_mov_b64 s[24:25], -1
	s_cbranch_vccnz .LBB0_463
	v_pk_mul_f32 v[52:53], v[44:45], v[44:45]
	v_pk_mul_f32 v[54:55], v[42:43], v[42:43]
	v_pk_fma_f32 v[52:53], v[48:49], v[48:49], v[52:53]
	v_pk_fma_f32 v[54:55], v[46:47], v[46:47], v[54:55]
	s_mov_b64 s[24:25], 0
	v_pk_mov_b32 v[56:57], v[54:55], v[52:53] op_sel:[1,0]
	v_mov_b32_e32 v55, v53
	v_pk_add_f32 v[52:53], v[56:57], v[54:55]
	v_lshlrev_b32_e32 v56, 1, v50
	v_add_f32_e32 v51, v52, v53
	v_cvt_pk_bf16_f32 v52, v46, v47
	v_cvt_pk_bf16_f32 v53, v48, v49
	v_cvt_pk_bf16_f32 v54, v42, v43
	v_cvt_pk_bf16_f32 v55, v44, v45
	global_store_dwordx4 v56, v[52:55], s[12:13]

; #define PG8_GAS __attribute__((address_space(1)))
; #define PG8_PACK8(y0, y1) (u32x4){cvt_pk_bf16((y0)[0], (y0)[1]), cvt_pk_bf16((y0)[2], (y0)[3]), cvt_pk_bf16((y1)[0], (y1)[1]), cvt_pk_bf16((y1)[2], (y1)[3])}
;     __device__ __forceinline__ void operator()(const f32x4 (&acc)[2][2][4][2], const Unit& u, int ui, int wr, int wc, int fr, int fq) const {
;     ...
;                 for (int bj = 0; bj < 2; ++bj) {
;                     const unsigned off = row * 1024u + col0 + bj * HALF;
;                     const u32x4 x4 = xw[ai][m][bj];
;                     f32x4 o0, o1;
;                     o0[0] = __builtin_bit_cast(float, x4[0] << 16) + acc[ai][bj][m][0][0]; o0[1] = __builtin_bit_cast(float, x4[0] & 0xffff0000u) + acc[ai][bj][m][0][1];
;                     o0[2] = __builtin_bit_cast(float, x4[1] << 16) + acc[ai][bj][m][0][2]; o0[3] = __builtin_bit_cast(float, x4[1] & 0xffff0000u) + acc[ai][bj][m][0][3];
;                     o1[0] = __builtin_bit_cast(float, x4[2] << 16) + acc[ai][bj][m][1][0]; o1[1] = __builtin_bit_cast(float, x4[2] & 0xffff0000u) + acc[ai][bj][m][1][1];
;                     o1[2] = __builtin_bit_cast(float, x4[3] << 16) + acc[ai][bj][m][1][2]; o1[3] = __builtin_bit_cast(float, x4[3] & 0xffff0000u) + acc[ai][bj][m][1][3];
;                     if (last) { __builtin_nontemporal_store(o0, (PG8_GAS f32x4*)((PG8_GAS float*)out + (size_t)off)); __builtin_nontemporal_store(o1, (PG8_GAS f32x4*)((PG8_GAS float*)out + (size_t)off + 4)); }
;                     else {
;                         const f32x4 q4 = o0 * o0 + o1 * o1; ss += (q4[0] + q4[1]) + (q4[2] + q4[3]);
;                         *(PG8_GAS u32x4*)((PG8_GAS unsigned char*)ws + E_XB + (size_t)(off * 2u)) = PG8_PACK8(o0, o1);
.LBB0_465:
	s_waitcnt vmcnt(15)
	v_lshlrev_b32_e32 v44, 16, v122
	v_and_b32_e32 v45, 0xffff0000, v122
	v_pk_add_f32 v[38:39], v[38:39], v[44:45]
	v_lshlrev_b32_e32 v44, 16, v123
	v_and_b32_e32 v45, 0xffff0000, v123
	v_pk_add_f32 v[40:41], v[40:41], v[44:45]
	v_lshlrev_b32_e32 v44, 16, v124
	v_and_b32_e32 v45, 0xffff0000, v124
	v_pk_add_f32 v[34:35], v[34:35], v[44:45]
	v_lshlrev_b32_e32 v44, 16, v125
	v_and_b32_e32 v45, 0xffff0000, v125
	v_add_u32_e32 v42, 0x24080, v0
	v_pk_add_f32 v[36:37], v[36:37], v[44:45]
	s_and_b64 vcc, exec, s[0:1]
	s_mov_b64 s[24:25], -1
	s_cbranch_vccnz .LBB0_467
	v_pk_mul_f32 v[44:45], v[36:37], v[36:37]
	v_pk_mul_f32 v[46:47], v[34:35], v[34:35]
	v_pk_fma_f32 v[44:45], v[40:41], v[40:41], v[44:45]
	v_pk_fma_f32 v[46:47], v[38:39], v[38:39], v[46:47]
	s_mov_b64 s[24:25], 0
	v_pk_mov_b32 v[48:49], v[46:47], v[44:45] op_sel:[1,0]
	v_mov_b32_e32 v47, v45
	v_pk_add_f32 v[44:45], v[48:49], v[46:47]
	v_lshlrev_b32_e32 v48, 1, v42
	v_add_f32_e32 v43, v44, v45
	v_add_f32_e32 v43, v43, v51
	v_cvt_pk_bf16_f32 v44, v38, v39
	v_cvt_pk_bf16_f32 v45, v40, v41
	v_cvt_pk_bf16_f32 v46, v34, v35
	v_cvt_pk_bf16_f32 v47, v36, v37
	global_store_dwordx4 v48, v[44:47], s[12:13]

; #define PG8_GAS __attribute__((address_space(1)))
; #define PG8_PACK8(y0, y1) (u32x4){cvt_pk_bf16((y0)[0], (y0)[1]), cvt_pk_bf16((y0)[2], (y0)[3]), cvt_pk_bf16((y1)[0], (y1)[1]), cvt_pk_bf16((y1)[2], (y1)[3])}
;     __device__ __forceinline__ void operator()(const f32x4 (&acc)[2][2][4][2], const Unit& u, int ui, int wr, int wc, int fr, int fq) const {
;     ...
;                 for (int bj = 0; bj < 2; ++bj) {
;                     const unsigned off = row * 1024u + col0 + bj * HALF;
;                     const u32x4 x4 = xw[ai][m][bj];
;                     f32x4 o0, o1;
;                     o0[0] = __builtin_bit_cast(float, x4[0] << 16) + acc[ai][bj][m][0][0]; o0[1] = __builtin_bit_cast(float, x4[0] & 0xffff0000u) + acc[ai][bj][m][0][1];
;                     o0[2] = __builtin_bit_cast(float, x4[1] << 16) + acc[ai][bj][m][0][2]; o0[3] = __builtin_bit_cast(float, x4[1] & 0xffff0000u) + acc[ai][bj][m][0][3];
;                     o1[0] = __builtin_bit_cast(float, x4[2] << 16) + acc[ai][bj][m][1][0]; o1[1] = __builtin_bit_cast(float, x4[2] & 0xffff0000u) + acc[ai][bj][m][1][1];
;                     o1[2] = __builtin_bit_cast(float, x4[3] << 16) + acc[ai][bj][m][1][2]; o1[3] = __builtin_bit_cast(float, x4[3] & 0xffff0000u) + acc[ai][bj][m][1][3];
;                     if (last) { __builtin_nontemporal_store(o0, (PG8_GAS f32x4*)((PG8_GAS float*)out + (size_t)off)); __builtin_nontemporal_store(o1, (PG8_GAS f32x4*)((PG8_GAS float*)out + (size_t)off + 4)); }
;                     else {
;                         const f32x4 q4 = o0 * o0 + o1 * o1; ss += (q4[0] + q4[1]) + (q4[2] + q4[3]);
;                         *(PG8_GAS u32x4*)((PG8_GAS unsigned char*)ws + E_XB + (size_t)(off * 2u)) = PG8_PACK8(o0, o1);
.LBB0_469:
	s_waitcnt vmcnt(15)
	v_lshlrev_b32_e32 v36, 16, v106
	v_and_b32_e32 v37, 0xffff0000, v106
	v_pk_add_f32 v[30:31], v[30:31], v[36:37]
	v_lshlrev_b32_e32 v36, 16, v107
	v_and_b32_e32 v37, 0xffff0000, v107
	v_pk_add_f32 v[32:33], v[32:33], v[36:37]
	v_lshlrev_b32_e32 v36, 16, v108
	v_and_b32_e32 v37, 0xffff0000, v108
	v_pk_add_f32 v[26:27], v[26:27], v[36:37]
	v_lshlrev_b32_e32 v36, 16, v109
	v_and_b32_e32 v37, 0xffff0000, v109
	v_add_u32_e32 v34, 0x28000, v0
	v_pk_add_f32 v[28:29], v[28:29], v[36:37]
	s_and_b64 vcc, exec, s[0:1]
	s_mov_b64 s[24:25], -1
	s_cbranch_vccnz .LBB0_471
	v_pk_mul_f32 v[36:37], v[28:29], v[28:29]
	v_pk_mul_f32 v[38:39], v[26:27], v[26:27]
	v_pk_fma_f32 v[36:37], v[32:33], v[32:33], v[36:37]
	v_pk_fma_f32 v[38:39], v[30:31], v[30:31], v[38:39]
	s_mov_b64 s[24:25], 0
	v_pk_mov_b32 v[40:41], v[38:39], v[36:37] op_sel:[1,0]
	v_mov_b32_e32 v39, v37
	v_pk_add_f32 v[36:37], v[40:41], v[38:39]
	v_lshlrev_b32_e32 v40, 1, v34
	v_add_f32_e32 v35, v36, v37
	v_cvt_pk_bf16_f32 v36, v30, v31
	v_cvt_pk_bf16_f32 v37, v32, v33
	v_cvt_pk_bf16_f32 v38, v26, v27
	v_cvt_pk_bf16_f32 v39, v28, v29
	global_store_dwordx4 v40, v[36:39], s[12:13]

; #define PG8_GAS __attribute__((address_space(1)))
; #define PG8_PACK8(y0, y1) (u32x4){cvt_pk_bf16((y0)[0], (y0)[1]), cvt_pk_bf16((y0)[2], (y0)[3]), cvt_pk_bf16((y1)[0], (y1)[1]), cvt_pk_bf16((y1)[2], (y1)[3])}
;     __device__ __forceinline__ void operator()(const f32x4 (&acc)[2][2][4][2], const Unit& u, int ui, int wr, int wc, int fr, int fq) const {
;     ...
;                 for (int bj = 0; bj < 2; ++bj) {
;                     const unsigned off = row * 1024u + col0 + bj * HALF;
;                     const u32x4 x4 = xw[ai][m][bj];
;                     f32x4 o0, o1;
;                     o0[0] = __builtin_bit_cast(float, x4[0] << 16) + acc[ai][bj][m][0][0]; o0[1] = __builtin_bit_cast(float, x4[0] & 0xffff0000u) + acc[ai][bj][m][0][1];
;                     o0[2] = __builtin_bit_cast(float, x4[1] << 16) + acc[ai][bj][m][0][2]; o0[3] = __builtin_bit_cast(float, x4[1] & 0xffff0000u) + acc[ai][bj][m][0][3];
;                     o1[0] = __builtin_bit_cast(float, x4[2] << 16) + acc[ai][bj][m][1][0]; o1[1] = __builtin_bit_cast(float, x4[2] & 0xffff0000u) + acc[ai][bj][m][1][1];
;                     o1[2] = __builtin_bit_cast(float, x4[3] << 16) + acc[ai][bj][m][1][2]; o1[3] = __builtin_bit_cast(float, x4[3] & 0xffff0000u) + acc[ai][bj][m][1][3];
;                     if (last) { __builtin_nontemporal_store(o0, (PG8_GAS f32x4*)((PG8_GAS float*)out + (size_t)off)); __builtin_nontemporal_store(o1, (PG8_GAS f32x4*)((PG8_GAS float*)out + (size_t)off + 4)); }
;                     else {
;                         const f32x4 q4 = o0 * o0 + o1 * o1; ss += (q4[0] + q4[1]) + (q4[2] + q4[3]);
;                         *(PG8_GAS u32x4*)((PG8_GAS unsigned char*)ws + E_XB + (size_t)(off * 2u)) = PG8_PACK8(o0, o1);
.LBB0_473:
	s_waitcnt vmcnt(15)
	v_lshlrev_b32_e32 v28, 16, v98
	v_and_b32_e32 v29, 0xffff0000, v98
	v_pk_add_f32 v[22:23], v[22:23], v[28:29]
	v_lshlrev_b32_e32 v28, 16, v99
	v_and_b32_e32 v29, 0xffff0000, v99
	v_pk_add_f32 v[24:25], v[24:25], v[28:29]
	v_lshlrev_b32_e32 v28, 16, v100
	v_and_b32_e32 v29, 0xffff0000, v100
	v_pk_add_f32 v[18:19], v[18:19], v[28:29]
	v_lshlrev_b32_e32 v28, 16, v101
	v_and_b32_e32 v29, 0xffff0000, v101
	v_add_u32_e32 v26, 0x28080, v0
	v_pk_add_f32 v[20:21], v[20:21], v[28:29]
	s_and_b64 vcc, exec, s[0:1]
	s_mov_b64 s[24:25], -1
	s_cbranch_vccnz .LBB0_475
	v_pk_mul_f32 v[28:29], v[20:21], v[20:21]
	v_pk_mul_f32 v[30:31], v[18:19], v[18:19]
	v_pk_fma_f32 v[28:29], v[24:25], v[24:25], v[28:29]
	v_pk_fma_f32 v[30:31], v[22:23], v[22:23], v[30:31]
	s_mov_b64 s[24:25], 0
	v_pk_mov_b32 v[32:33], v[30:31], v[28:29] op_sel:[1,0]
	v_mov_b32_e32 v31, v29
	v_pk_add_f32 v[28:29], v[32:33], v[30:31]
	v_lshlrev_b32_e32 v32, 1, v26
	v_add_f32_e32 v27, v28, v29
	v_add_f32_e32 v27, v27, v35
	v_cvt_pk_bf16_f32 v28, v22, v23
	v_cvt_pk_bf16_f32 v29, v24, v25
	v_cvt_pk_bf16_f32 v30, v18, v19
	v_cvt_pk_bf16_f32 v31, v20, v21
	global_store_dwordx4 v32, v[28:31], s[12:13]

; #define PG8_GAS __attribute__((address_space(1)))
; #define PG8_PACK8(y0, y1) (u32x4){cvt_pk_bf16((y0)[0], (y0)[1]), cvt_pk_bf16((y0)[2], (y0)[3]), cvt_pk_bf16((y1)[0], (y1)[1]), cvt_pk_bf16((y1)[2], (y1)[3])}
;     __device__ __forceinline__ void operator()(const f32x4 (&acc)[2][2][4][2], const Unit& u, int ui, int wr, int wc, int fr, int fq) const {
;     ...
;                 for (int bj = 0; bj < 2; ++bj) {
;                     const unsigned off = row * 1024u + col0 + bj * HALF;
;                     const u32x4 x4 = xw[ai][m][bj];
;                     f32x4 o0, o1;
;                     o0[0] = __builtin_bit_cast(float, x4[0] << 16) + acc[ai][bj][m][0][0]; o0[1] = __builtin_bit_cast(float, x4[0] & 0xffff0000u) + acc[ai][bj][m][0][1];
;                     o0[2] = __builtin_bit_cast(float, x4[1] << 16) + acc[ai][bj][m][0][2]; o0[3] = __builtin_bit_cast(float, x4[1] & 0xffff0000u) + acc[ai][bj][m][0][3];
;                     o1[0] = __builtin_bit_cast(float, x4[2] << 16) + acc[ai][bj][m][1][0]; o1[1] = __builtin_bit_cast(float, x4[2] & 0xffff0000u) + acc[ai][bj][m][1][1];
;                     o1[2] = __builtin_bit_cast(float, x4[3] << 16) + acc[ai][bj][m][1][2]; o1[3] = __builtin_bit_cast(float, x4[3] & 0xffff0000u) + acc[ai][bj][m][1][3];
;                     if (last) { __builtin_nontemporal_store(o0, (PG8_GAS f32x4*)((PG8_GAS float*)out + (size_t)off)); __builtin_nontemporal_store(o1, (PG8_GAS f32x4*)((PG8_GAS float*)out + (size_t)off + 4)); }
;                     else {
;                         const f32x4 q4 = o0 * o0 + o1 * o1; ss += (q4[0] + q4[1]) + (q4[2] + q4[3]);
;                         *(PG8_GAS u32x4*)((PG8_GAS unsigned char*)ws + E_XB + (size_t)(off * 2u)) = PG8_PACK8(o0, o1);
.LBB0_477:
	s_waitcnt vmcnt(15)
	v_lshlrev_b32_e32 v20, 16, v86
	v_and_b32_e32 v21, 0xffff0000, v86
	v_pk_add_f32 v[14:15], v[14:15], v[20:21]
	v_lshlrev_b32_e32 v20, 16, v87
	v_and_b32_e32 v21, 0xffff0000, v87
	v_pk_add_f32 v[16:17], v[16:17], v[20:21]
	v_lshlrev_b32_e32 v20, 16, v88
	v_and_b32_e32 v21, 0xffff0000, v88
	v_pk_add_f32 v[10:11], v[10:11], v[20:21]
	v_lshlrev_b32_e32 v20, 16, v89
	v_and_b32_e32 v21, 0xffff0000, v89
	v_add_u32_e32 v18, 0x2c000, v0
	v_pk_add_f32 v[12:13], v[12:13], v[20:21]
	s_and_b64 vcc, exec, s[0:1]
	s_mov_b64 s[24:25], -1
	s_cbranch_vccnz .LBB0_479
	v_pk_mul_f32 v[20:21], v[12:13], v[12:13]
	v_pk_mul_f32 v[22:23], v[10:11], v[10:11]
	v_pk_fma_f32 v[20:21], v[16:17], v[16:17], v[20:21]
	v_pk_fma_f32 v[22:23], v[14:15], v[14:15], v[22:23]
	s_mov_b64 s[24:25], 0
	v_pk_mov_b32 v[24:25], v[22:23], v[20:21] op_sel:[1,0]
	v_mov_b32_e32 v23, v21
	v_pk_add_f32 v[20:21], v[24:25], v[22:23]
	v_lshlrev_b32_e32 v24, 1, v18
	v_add_f32_e32 v19, v20, v21
	v_cvt_pk_bf16_f32 v20, v14, v15
	v_cvt_pk_bf16_f32 v21, v16, v17
	v_cvt_pk_bf16_f32 v22, v10, v11
	v_cvt_pk_bf16_f32 v23, v12, v13
	global_store_dwordx4 v24, v[20:23], s[12:13]

; #define PG8_GAS __attribute__((address_space(1)))
; #define PG8_PACK8(y0, y1) (u32x4){cvt_pk_bf16((y0)[0], (y0)[1]), cvt_pk_bf16((y0)[2], (y0)[3]), cvt_pk_bf16((y1)[0], (y1)[1]), cvt_pk_bf16((y1)[2], (y1)[3])}
;     __device__ __forceinline__ void operator()(const f32x4 (&acc)[2][2][4][2], const Unit& u, int ui, int wr, int wc, int fr, int fq) const {
;     ...
;                 for (int bj = 0; bj < 2; ++bj) {
;                     const unsigned off = row * 1024u + col0 + bj * HALF;
;                     const u32x4 x4 = xw[ai][m][bj];
;                     f32x4 o0, o1;
;                     o0[0] = __builtin_bit_cast(float, x4[0] << 16) + acc[ai][bj][m][0][0]; o0[1] = __builtin_bit_cast(float, x4[0] & 0xffff0000u) + acc[ai][bj][m][0][1];
;                     o0[2] = __builtin_bit_cast(float, x4[1] << 16) + acc[ai][bj][m][0][2]; o0[3] = __builtin_bit_cast(float, x4[1] & 0xffff0000u) + acc[ai][bj][m][0][3];
;                     o1[0] = __builtin_bit_cast(float, x4[2] << 16) + acc[ai][bj][m][1][0]; o1[1] = __builtin_bit_cast(float, x4[2] & 0xffff0000u) + acc[ai][bj][m][1][1];
;                     o1[2] = __builtin_bit_cast(float, x4[3] << 16) + acc[ai][bj][m][1][2]; o1[3] = __builtin_bit_cast(float, x4[3] & 0xffff0000u) + acc[ai][bj][m][1][3];
;                     if (last) { __builtin_nontemporal_store(o0, (PG8_GAS f32x4*)((PG8_GAS float*)out + (size_t)off)); __builtin_nontemporal_store(o1, (PG8_GAS f32x4*)((PG8_GAS float*)out + (size_t)off + 4)); }
;                     else {
;                         const f32x4 q4 = o0 * o0 + o1 * o1; ss += (q4[0] + q4[1]) + (q4[2] + q4[3]);
;                         *(PG8_GAS u32x4*)((PG8_GAS unsigned char*)ws + E_XB + (size_t)(off * 2u)) = PG8_PACK8(o0, o1);
.LBB0_481:
	s_waitcnt vmcnt(15)
	v_lshlrev_b32_e32 v10, 16, v74
	v_and_b32_e32 v11, 0xffff0000, v74
	v_pk_add_f32 v[6:7], v[6:7], v[10:11]
	v_lshlrev_b32_e32 v10, 16, v75
	v_and_b32_e32 v11, 0xffff0000, v75
	v_pk_add_f32 v[8:9], v[8:9], v[10:11]
	v_lshlrev_b32_e32 v10, 16, v76
	v_and_b32_e32 v11, 0xffff0000, v76
	v_pk_add_f32 v[2:3], v[2:3], v[10:11]
	v_lshlrev_b32_e32 v10, 16, v77
	v_and_b32_e32 v11, 0xffff0000, v77
	v_add_u32_e32 v0, 0x2c080, v0
	v_pk_add_f32 v[4:5], v[4:5], v[10:11]
	s_and_b64 vcc, exec, s[0:1]
	s_mov_b64 s[24:25], -1
	s_cbranch_vccnz .LBB0_487
	v_pk_mul_f32 v[10:11], v[4:5], v[4:5]
	v_pk_mul_f32 v[12:13], v[2:3], v[2:3]
	v_pk_fma_f32 v[10:11], v[8:9], v[8:9], v[10:11]
	v_pk_fma_f32 v[12:13], v[6:7], v[6:7], v[12:13]
	s_nop 0
	v_pk_mov_b32 v[14:15], v[12:13], v[10:11] op_sel:[1,0]
	v_mov_b32_e32 v13, v11
	v_pk_add_f32 v[10:11], v[14:15], v[12:13]
	v_cvt_pk_bf16_f32 v12, v6, v7
	v_cvt_pk_bf16_f32 v13, v8, v9
	v_cvt_pk_bf16_f32 v14, v2, v3
	v_cvt_pk_bf16_f32 v15, v4, v5
	s_nop 0
	v_add_f32_e32 v10, v10, v11
	v_add_f32_e32 v10, v10, v19
	v_lshlrev_b32_e32 v11, 1, v0
	global_store_dwordx4 v11, v[12:15], s[12:13]
	s_cbranch_execz .LBB0_488

; __global__ void __launch_bounds__(NWAVES * 64, 2) mk_fwd(Args args) {
;     __shared__ __attribute__((aligned(16))) unsigned char lds[LDS_BYTES];
	.amdhsa_kernel _Z6mk_fwd4Args
		.amdhsa_group_segment_fixed_size 163840
		.amdhsa_private_segment_fixed_size 0
		.amdhsa_kernarg_size 368
		.amdhsa_user_sgpr_count 2
		.amdhsa_user_sgpr_dispatch_ptr 0
		.amdhsa_user_sgpr_queue_ptr 0
		.amdhsa_user_sgpr_kernarg_segment_ptr 1
		.amdhsa_user_sgpr_dispatch_id 0
		.amdhsa_user_sgpr_kernarg_preload_length 0
		.amdhsa_user_sgpr_kernarg_preload_offset 0
		.amdhsa_user_sgpr_private_segment_size 0
		.amdhsa_uses_dynamic_stack 0
		.amdhsa_enable_private_segment 0
		.amdhsa_system_sgpr_workgroup_id_x 1
		.amdhsa_system_sgpr_workgroup_id_y 0
		.amdhsa_system_sgpr_workgroup_id_z 0
		.amdhsa_system_sgpr_workgroup_info 0
		.amdhsa_system_vgpr_workitem_id 0
		.amdhsa_next_free_vgpr 256
		.amdhsa_next_free_sgpr 102
		.amdhsa_accum_offset 256
		.amdhsa_reserve_vcc 1
		.amdhsa_float_round_mode_32 0
		.amdhsa_float_round_mode_16_64 0
		.amdhsa_float_denorm_mode_32 3
		.amdhsa_float_denorm_mode_16_64 3
		.amdhsa_dx10_clamp 1
		.amdhsa_ieee_mode 1
		.amdhsa_fp16_overflow 0
		.amdhsa_tg_split 0
		.amdhsa_exception_fp_ieee_invalid_op 0
		.amdhsa_exception_fp_denorm_src 0
		.amdhsa_exception_fp_ieee_div_zero 0
		.amdhsa_exception_fp_ieee_overflow 0
		.amdhsa_exception_fp_ieee_underflow 0
		.amdhsa_exception_fp_ieee_inexact 0
		.amdhsa_exception_int_div_zero 0
	.end_amdhsa_kernel

; __global__ void __launch_bounds__(NWAVES * 64, 2) mk_fwd(Args args) {
;     __shared__ __attribute__((aligned(16))) unsigned char lds[LDS_BYTES];
amdhsa.kernels:
  - .agpr_count:     0
    .args:
      - .offset:         0
        .size:           112
        .value_kind:     by_value
      - .offset:         112
        .size:           4
        .value_kind:     hidden_block_count_x
      - .offset:         116
        .size:           4
        .value_kind:     hidden_block_count_y
      - .offset:         120
        .size:           4
        .value_kind:     hidden_block_count_z
      - .offset:         124
        .size:           2
        .value_kind:     hidden_group_size_x
      - .offset:         126
        .size:           2
        .value_kind:     hidden_group_size_y
      - .offset:         128
        .size:           2
        .value_kind:     hidden_group_size_z
      - .offset:         130
        .size:           2
        .value_kind:     hidden_remainder_x
      - .offset:         132
        .size:           2
        .value_kind:     hidden_remainder_y
      - .offset:         134
        .size:           2
        .value_kind:     hidden_remainder_z
      - .offset:         152
        .size:           8
        .value_kind:     hidden_global_offset_x
      - .offset:         160
        .size:           8
        .value_kind:     hidden_global_offset_y
      - .offset:         168
        .size:           8
        .value_kind:     hidden_global_offset_z
      - .offset:         176
        .size:           2
        .value_kind:     hidden_grid_dims
    .group_segment_fixed_size: 163840
    .kernarg_segment_align: 8
    .kernarg_segment_size: 368
    .language:       OpenCL C
    .language_version:
      - 2
      - 0
    .max_flat_workgroup_size: 512
    .name:           _Z6mk_fwd4Args
    .private_segment_fixed_size: 0
    .sgpr_count:     108
    .sgpr_spill_count: 240
    .symbol:         _Z6mk_fwd4Args.kd
    .uniform_work_group_size: 1
    .uses_dynamic_stack: false
    .vgpr_count:     256
    .vgpr_spill_count: 0
    .wavefront_size: 64
